# router LN gain/bias staged in LDS (ds_read instead of global loads, chain waits on lgkmcnt only) on top of vm10+womap+nop
# baseline (speedup 1.0000x reference)
; #define OPAQUE_TID(P) (((P).wid0 << 6) | lane_id_now())
; template <bool DRY = false>
; DI void phase_ln_router(const Params& p, char* smem, int bid, int nb) {
;   float* hs = (float*)smem;
;   float* red = hs + 8 * 2048;
;   float* lg = red + 32 * 8 * 32;
;   int* lcnt = (int*)(lg + 8 * 32);
;   int* lbase = lcnt + 32;
;   int* lasg = lbase + 32;
;   int* lnum = lasg + 1024;
;   float* lgate = (float*)(lnum + 4);
;   const int tid = OPAQUE_TID(p), lane = tid & 63, wv = tid >> 6;
;   const int e = tid & 15, ks = tid >> 4;
;   f32x2_t wr[64];
; #pragma unroll
;   for (int i = 0; i < 64; ++i) { wr[i][0] = p.w_router[(size_t)(ks * 64 + i) * 32 + e]; wr[i][1] = p.w_router[(size_t)(ks * 64 + i) * 32 + e + 16]; }
.LBB0_1322:
	s_or_b64 exec, exec, s[0:1]
	s_waitcnt lgkmcnt(0)
	s_barrier
	v_mbcnt_lo_u32_b32 v6, -1, 0
	v_mbcnt_hi_u32_b32 v6, -1, v6
	v_readlane_b32 s0, v254, 19
	v_or_b32_e32 v200, s87, v6
	v_ashrrev_i32_e32 v7, 4, v200
	v_and_b32_e32 v136, 15, v6
	v_lshlrev_b32_e32 v2, 6, v7
	v_lshlrev_b32_e32 v0, 2, v136
	v_mov_b32_e32 v1, 0
	v_readlane_b32 s12, v254, 31
	v_readlane_b32 s13, v254, 32
	v_ashrrev_i32_e32 v3, 31, v2
	v_lshlrev_b64 v[8:9], 7, v[2:3]
	v_lshl_add_u64 v[4:5], s[12:13], 0, v[0:1]
	v_lshl_add_u64 v[16:17], v[4:5], 0, v[8:9]
	v_or_b32_e32 v8, 1, v2
	v_ashrrev_i32_e32 v9, 31, v8
	v_lshlrev_b64 v[8:9], 7, v[8:9]
	v_lshl_add_u64 v[18:19], v[4:5], 0, v[8:9]
	v_or_b32_e32 v8, 2, v2
	v_ashrrev_i32_e32 v9, 31, v8
	v_lshlrev_b64 v[8:9], 7, v[8:9]
	v_lshl_add_u64 v[20:21], v[4:5], 0, v[8:9]
	v_or_b32_e32 v8, 3, v2
	v_ashrrev_i32_e32 v9, 31, v8
	v_lshlrev_b64 v[8:9], 7, v[8:9]
	v_lshl_add_u64 v[22:23], v[4:5], 0, v[8:9]
	global_load_dword v8, v[16:17], off
	global_load_dword v9, v[16:17], off offset:64
	global_load_dword v10, v[18:19], off
	global_load_dword v11, v[18:19], off offset:64
	global_load_dword v12, v[20:21], off
	global_load_dword v13, v[20:21], off offset:64
	global_load_dword v14, v[22:23], off
	global_load_dword v15, v[22:23], off offset:64
	v_or_b32_e32 v16, 4, v2
	v_ashrrev_i32_e32 v17, 31, v16
	v_lshlrev_b64 v[16:17], 7, v[16:17]
	v_lshl_add_u64 v[24:25], v[4:5], 0, v[16:17]
	v_or_b32_e32 v16, 5, v2
	v_ashrrev_i32_e32 v17, 31, v16
	v_lshlrev_b64 v[16:17], 7, v[16:17]
	v_lshl_add_u64 v[26:27], v[4:5], 0, v[16:17]
	v_or_b32_e32 v16, 6, v2
	v_ashrrev_i32_e32 v17, 31, v16
	v_lshlrev_b64 v[16:17], 7, v[16:17]
	v_lshl_add_u64 v[28:29], v[4:5], 0, v[16:17]
	v_or_b32_e32 v16, 7, v2
	v_ashrrev_i32_e32 v17, 31, v16
	v_lshlrev_b64 v[16:17], 7, v[16:17]
	v_lshl_add_u64 v[30:31], v[4:5], 0, v[16:17]
	global_load_dword v16, v[24:25], off
	global_load_dword v17, v[24:25], off offset:64
	global_load_dword v18, v[26:27], off
	global_load_dword v19, v[26:27], off offset:64
	global_load_dword v20, v[28:29], off
	global_load_dword v21, v[28:29], off offset:64
	global_load_dword v22, v[30:31], off
	global_load_dword v23, v[30:31], off offset:64
	v_or_b32_e32 v24, 8, v2
	v_ashrrev_i32_e32 v25, 31, v24
	v_lshlrev_b64 v[24:25], 7, v[24:25]
	v_lshl_add_u64 v[32:33], v[4:5], 0, v[24:25]
	v_or_b32_e32 v24, 9, v2
	v_ashrrev_i32_e32 v25, 31, v24
	v_lshlrev_b64 v[24:25], 7, v[24:25]
	v_lshl_add_u64 v[34:35], v[4:5], 0, v[24:25]
	v_or_b32_e32 v24, 10, v2
	v_ashrrev_i32_e32 v25, 31, v24
	v_lshlrev_b64 v[24:25], 7, v[24:25]
	v_lshl_add_u64 v[36:37], v[4:5], 0, v[24:25]
	v_or_b32_e32 v24, 11, v2
	v_ashrrev_i32_e32 v25, 31, v24
	v_lshlrev_b64 v[24:25], 7, v[24:25]
	v_lshl_add_u64 v[38:39], v[4:5], 0, v[24:25]
	global_load_dword v24, v[32:33], off
	global_load_dword v25, v[32:33], off offset:64
	global_load_dword v26, v[34:35], off
	global_load_dword v27, v[34:35], off offset:64
	global_load_dword v28, v[36:37], off
	global_load_dword v29, v[36:37], off offset:64
	global_load_dword v30, v[38:39], off
	global_load_dword v31, v[38:39], off offset:64
	v_or_b32_e32 v32, 12, v2
	v_ashrrev_i32_e32 v33, 31, v32
	v_lshlrev_b64 v[32:33], 7, v[32:33]
	v_lshl_add_u64 v[40:41], v[4:5], 0, v[32:33]
	v_or_b32_e32 v32, 13, v2
	v_ashrrev_i32_e32 v33, 31, v32
	v_lshlrev_b64 v[32:33], 7, v[32:33]
	v_lshl_add_u64 v[42:43], v[4:5], 0, v[32:33]
	v_or_b32_e32 v32, 14, v2
	v_ashrrev_i32_e32 v33, 31, v32
	v_lshlrev_b64 v[32:33], 7, v[32:33]
	v_lshl_add_u64 v[44:45], v[4:5], 0, v[32:33]
	v_or_b32_e32 v32, 15, v2
	v_ashrrev_i32_e32 v33, 31, v32
	v_lshlrev_b64 v[32:33], 7, v[32:33]
	v_lshl_add_u64 v[46:47], v[4:5], 0, v[32:33]
	global_load_dword v32, v[40:41], off
	global_load_dword v33, v[40:41], off offset:64
	global_load_dword v34, v[42:43], off
	global_load_dword v35, v[42:43], off offset:64
	global_load_dword v36, v[44:45], off
	global_load_dword v37, v[44:45], off offset:64
	global_load_dword v38, v[46:47], off
	global_load_dword v39, v[46:47], off offset:64
	v_or_b32_e32 v40, 16, v2
	v_ashrrev_i32_e32 v41, 31, v40
	v_lshlrev_b64 v[40:41], 7, v[40:41]
	v_lshl_add_u64 v[48:49], v[4:5], 0, v[40:41]
	v_or_b32_e32 v40, 17, v2
	v_ashrrev_i32_e32 v41, 31, v40
	v_lshlrev_b64 v[40:41], 7, v[40:41]
	v_lshl_add_u64 v[50:51], v[4:5], 0, v[40:41]
	v_or_b32_e32 v40, 18, v2
	v_ashrrev_i32_e32 v41, 31, v40
	v_lshlrev_b64 v[40:41], 7, v[40:41]
	v_lshl_add_u64 v[52:53], v[4:5], 0, v[40:41]
	v_or_b32_e32 v40, 19, v2
	v_ashrrev_i32_e32 v41, 31, v40
	v_lshlrev_b64 v[40:41], 7, v[40:41]
	v_lshl_add_u64 v[54:55], v[4:5], 0, v[40:41]
	global_load_dword v40, v[48:49], off
	global_load_dword v41, v[48:49], off offset:64
	global_load_dword v42, v[50:51], off
	global_load_dword v43, v[50:51], off offset:64
	global_load_dword v44, v[52:53], off
	global_load_dword v45, v[52:53], off offset:64
	global_load_dword v46, v[54:55], off
	global_load_dword v47, v[54:55], off offset:64
	v_or_b32_e32 v48, 20, v2
	v_ashrrev_i32_e32 v49, 31, v48
	v_lshlrev_b64 v[48:49], 7, v[48:49]
	v_lshl_add_u64 v[56:57], v[4:5], 0, v[48:49]
	v_or_b32_e32 v48, 21, v2
	v_ashrrev_i32_e32 v49, 31, v48
	v_lshlrev_b64 v[48:49], 7, v[48:49]
	v_lshl_add_u64 v[58:59], v[4:5], 0, v[48:49]
	v_or_b32_e32 v48, 22, v2
	v_ashrrev_i32_e32 v49, 31, v48
	v_lshlrev_b64 v[48:49], 7, v[48:49]
	v_lshl_add_u64 v[60:61], v[4:5], 0, v[48:49]
	v_or_b32_e32 v48, 23, v2
	v_ashrrev_i32_e32 v49, 31, v48
	v_lshlrev_b64 v[48:49], 7, v[48:49]
	v_lshl_add_u64 v[62:63], v[4:5], 0, v[48:49]
	global_load_dword v48, v[56:57], off
	global_load_dword v49, v[56:57], off offset:64
	global_load_dword v50, v[58:59], off
	global_load_dword v51, v[58:59], off offset:64
; template <bool DRY = false>
; DI void phase_ln_router(const Params& p, char* smem, int bid, int nb) {
;     ...
;   f32x2_t wr[64];
; #pragma unroll
;   for (int i = 0; i < 64; ++i) { wr[i][0] = p.w_router[(size_t)(ks * 64 + i) * 32 + e]; wr[i][1] = p.w_router[(size_t)(ks * 64 + i) * 32 + e + 16]; }
	global_load_dword v52, v[60:61], off
	global_load_dword v53, v[60:61], off offset:64
	global_load_dword v54, v[62:63], off
	global_load_dword v55, v[62:63], off offset:64
	v_or_b32_e32 v56, 24, v2
	v_ashrrev_i32_e32 v57, 31, v56
	v_lshlrev_b64 v[56:57], 7, v[56:57]
	v_lshl_add_u64 v[64:65], v[4:5], 0, v[56:57]
	v_or_b32_e32 v56, 25, v2
	v_ashrrev_i32_e32 v57, 31, v56
	v_lshlrev_b64 v[56:57], 7, v[56:57]
	v_lshl_add_u64 v[66:67], v[4:5], 0, v[56:57]
	v_or_b32_e32 v56, 26, v2
	v_ashrrev_i32_e32 v57, 31, v56
	v_lshlrev_b64 v[56:57], 7, v[56:57]
	v_lshl_add_u64 v[68:69], v[4:5], 0, v[56:57]
	v_or_b32_e32 v56, 27, v2
	v_ashrrev_i32_e32 v57, 31, v56
	v_lshlrev_b64 v[56:57], 7, v[56:57]
	v_lshl_add_u64 v[70:71], v[4:5], 0, v[56:57]
	global_load_dword v56, v[64:65], off
	global_load_dword v57, v[64:65], off offset:64
	global_load_dword v58, v[66:67], off
	global_load_dword v59, v[66:67], off offset:64
	global_load_dword v60, v[68:69], off
	global_load_dword v61, v[68:69], off offset:64
	global_load_dword v62, v[70:71], off
	global_load_dword v63, v[70:71], off offset:64
	v_or_b32_e32 v64, 28, v2
	v_ashrrev_i32_e32 v65, 31, v64
	v_lshlrev_b64 v[64:65], 7, v[64:65]
	v_lshl_add_u64 v[72:73], v[4:5], 0, v[64:65]
	v_or_b32_e32 v64, 29, v2
	v_ashrrev_i32_e32 v65, 31, v64
	v_lshlrev_b64 v[64:65], 7, v[64:65]
	v_lshl_add_u64 v[74:75], v[4:5], 0, v[64:65]
	v_or_b32_e32 v64, 30, v2
	v_ashrrev_i32_e32 v65, 31, v64
	v_lshlrev_b64 v[64:65], 7, v[64:65]
	v_lshl_add_u64 v[76:77], v[4:5], 0, v[64:65]
	v_or_b32_e32 v64, 31, v2
	v_ashrrev_i32_e32 v65, 31, v64
	v_lshlrev_b64 v[64:65], 7, v[64:65]
	v_lshl_add_u64 v[78:79], v[4:5], 0, v[64:65]
	global_load_dword v64, v[72:73], off
	global_load_dword v65, v[72:73], off offset:64
	global_load_dword v66, v[74:75], off
	global_load_dword v67, v[74:75], off offset:64
	global_load_dword v68, v[76:77], off
	global_load_dword v69, v[76:77], off offset:64
	global_load_dword v70, v[78:79], off
	global_load_dword v71, v[78:79], off offset:64
	v_or_b32_e32 v72, 32, v2
	v_ashrrev_i32_e32 v73, 31, v72
	v_lshlrev_b64 v[72:73], 7, v[72:73]
	v_lshl_add_u64 v[80:81], v[4:5], 0, v[72:73]
	v_or_b32_e32 v72, 33, v2
	v_ashrrev_i32_e32 v73, 31, v72
	v_lshlrev_b64 v[72:73], 7, v[72:73]
	s_waitcnt vmcnt(62)
	v_lshl_add_u64 v[82:83], v[4:5], 0, v[72:73]
	v_or_b32_e32 v72, 34, v2
	v_ashrrev_i32_e32 v73, 31, v72
	v_lshlrev_b64 v[72:73], 7, v[72:73]
	v_lshl_add_u64 v[84:85], v[4:5], 0, v[72:73]
	v_or_b32_e32 v72, 35, v2
	v_ashrrev_i32_e32 v73, 31, v72
	v_lshlrev_b64 v[72:73], 7, v[72:73]
	v_lshl_add_u64 v[86:87], v[4:5], 0, v[72:73]
	global_load_dword v72, v[80:81], off
	global_load_dword v73, v[80:81], off offset:64
	global_load_dword v74, v[82:83], off
	global_load_dword v75, v[82:83], off offset:64
	global_load_dword v76, v[84:85], off
	global_load_dword v77, v[84:85], off offset:64
	global_load_dword v78, v[86:87], off
	global_load_dword v79, v[86:87], off offset:64
	v_or_b32_e32 v80, 36, v2
	v_ashrrev_i32_e32 v81, 31, v80
	v_lshlrev_b64 v[80:81], 7, v[80:81]
	v_lshl_add_u64 v[88:89], v[4:5], 0, v[80:81]
	v_or_b32_e32 v80, 37, v2
	v_ashrrev_i32_e32 v81, 31, v80
	v_lshlrev_b64 v[80:81], 7, v[80:81]
	v_lshl_add_u64 v[90:91], v[4:5], 0, v[80:81]
	v_or_b32_e32 v80, 38, v2
	v_ashrrev_i32_e32 v81, 31, v80
	v_lshlrev_b64 v[80:81], 7, v[80:81]
	v_lshl_add_u64 v[92:93], v[4:5], 0, v[80:81]
	v_or_b32_e32 v80, 39, v2
	v_ashrrev_i32_e32 v81, 31, v80
	v_lshlrev_b64 v[80:81], 7, v[80:81]
	v_lshl_add_u64 v[94:95], v[4:5], 0, v[80:81]
	global_load_dword v80, v[88:89], off
	global_load_dword v81, v[88:89], off offset:64
	global_load_dword v82, v[90:91], off
	global_load_dword v83, v[90:91], off offset:64
	global_load_dword v84, v[92:93], off
	global_load_dword v85, v[92:93], off offset:64
	global_load_dword v86, v[94:95], off
	global_load_dword v87, v[94:95], off offset:64
	v_or_b32_e32 v88, 40, v2
	v_ashrrev_i32_e32 v89, 31, v88
	v_lshlrev_b64 v[88:89], 7, v[88:89]
	v_lshl_add_u64 v[96:97], v[4:5], 0, v[88:89]
	v_or_b32_e32 v88, 41, v2
	v_ashrrev_i32_e32 v89, 31, v88
	v_lshlrev_b64 v[88:89], 7, v[88:89]
	v_lshl_add_u64 v[98:99], v[4:5], 0, v[88:89]
	v_or_b32_e32 v88, 42, v2
	v_ashrrev_i32_e32 v89, 31, v88
	v_lshlrev_b64 v[88:89], 7, v[88:89]
	v_lshl_add_u64 v[100:101], v[4:5], 0, v[88:89]
	v_or_b32_e32 v88, 43, v2
	v_ashrrev_i32_e32 v89, 31, v88
	v_lshlrev_b64 v[88:89], 7, v[88:89]
	v_lshl_add_u64 v[102:103], v[4:5], 0, v[88:89]
	global_load_dword v88, v[96:97], off
	global_load_dword v89, v[96:97], off offset:64
	global_load_dword v90, v[98:99], off
	global_load_dword v91, v[98:99], off offset:64
	global_load_dword v92, v[100:101], off
	global_load_dword v93, v[100:101], off offset:64
	global_load_dword v94, v[102:103], off
	global_load_dword v95, v[102:103], off offset:64
	v_or_b32_e32 v96, 44, v2
	v_ashrrev_i32_e32 v97, 31, v96
	v_lshlrev_b64 v[96:97], 7, v[96:97]
	v_lshl_add_u64 v[104:105], v[4:5], 0, v[96:97]
	v_or_b32_e32 v96, 45, v2
	v_ashrrev_i32_e32 v97, 31, v96
	v_lshlrev_b64 v[96:97], 7, v[96:97]
	v_lshl_add_u64 v[106:107], v[4:5], 0, v[96:97]
	v_or_b32_e32 v96, 46, v2
	v_ashrrev_i32_e32 v97, 31, v96
	v_lshlrev_b64 v[96:97], 7, v[96:97]
	v_lshl_add_u64 v[108:109], v[4:5], 0, v[96:97]
	v_or_b32_e32 v96, 47, v2
	v_ashrrev_i32_e32 v97, 31, v96
	v_lshlrev_b64 v[96:97], 7, v[96:97]
	v_lshl_add_u64 v[110:111], v[4:5], 0, v[96:97]
	global_load_dword v96, v[104:105], off
	global_load_dword v97, v[104:105], off offset:64
	global_load_dword v98, v[106:107], off
	global_load_dword v99, v[106:107], off offset:64
	global_load_dword v100, v[108:109], off
	global_load_dword v101, v[108:109], off offset:64
	global_load_dword v102, v[110:111], off
; template <bool DRY = false>
; DI void phase_ln_router(const Params& p, char* smem, int bid, int nb) {
;     ...
;   f32x2_t wr[64];
; #pragma unroll
;   for (int i = 0; i < 64; ++i) { wr[i][0] = p.w_router[(size_t)(ks * 64 + i) * 32 + e]; wr[i][1] = p.w_router[(size_t)(ks * 64 + i) * 32 + e + 16]; }
;   if (tid < 32) lcnt[tid] = 0;
;   if (tid == 32) lnum[0] = 0;
;   __syncthreads();
;   u32x2 za[8];
;   {
;     const int tf = bid * 8 + wv;
;     const bf16_t* zr = p.z1b + (size_t)(tf < NTOK ? tf : 0) * DM;
; #pragma unroll
;     for (int i = 0; i < 8; ++i) za[i] = *(const u32x2*)(zr + (i * 64 + lane) * 4);
;   }
;   for (int t0 = bid * 8; t0 < NTOK; t0 += nb * 8) {
	global_load_dword v103, v[110:111], off offset:64
	v_or_b32_e32 v104, 48, v2
	v_ashrrev_i32_e32 v105, 31, v104
	v_lshlrev_b64 v[104:105], 7, v[104:105]
	v_lshl_add_u64 v[112:113], v[4:5], 0, v[104:105]
	v_or_b32_e32 v104, 49, v2
	v_ashrrev_i32_e32 v105, 31, v104
	v_lshlrev_b64 v[104:105], 7, v[104:105]
	v_lshl_add_u64 v[114:115], v[4:5], 0, v[104:105]
	v_or_b32_e32 v104, 50, v2
	v_ashrrev_i32_e32 v105, 31, v104
	v_lshlrev_b64 v[104:105], 7, v[104:105]
	v_lshl_add_u64 v[116:117], v[4:5], 0, v[104:105]
	v_or_b32_e32 v104, 51, v2
	v_ashrrev_i32_e32 v105, 31, v104
	v_lshlrev_b64 v[104:105], 7, v[104:105]
	v_lshl_add_u64 v[118:119], v[4:5], 0, v[104:105]
	global_load_dword v104, v[112:113], off
	global_load_dword v105, v[112:113], off offset:64
	global_load_dword v106, v[114:115], off
	global_load_dword v107, v[114:115], off offset:64
	global_load_dword v108, v[116:117], off
	global_load_dword v109, v[116:117], off offset:64
	global_load_dword v110, v[118:119], off
	global_load_dword v111, v[118:119], off offset:64
	v_or_b32_e32 v112, 52, v2
	v_ashrrev_i32_e32 v113, 31, v112
	v_lshlrev_b64 v[112:113], 7, v[112:113]
	v_lshl_add_u64 v[120:121], v[4:5], 0, v[112:113]
	v_or_b32_e32 v112, 53, v2
	v_ashrrev_i32_e32 v113, 31, v112
	v_lshlrev_b64 v[112:113], 7, v[112:113]
	v_lshl_add_u64 v[122:123], v[4:5], 0, v[112:113]
	v_or_b32_e32 v112, 54, v2
	v_ashrrev_i32_e32 v113, 31, v112
	v_lshlrev_b64 v[112:113], 7, v[112:113]
	v_lshl_add_u64 v[124:125], v[4:5], 0, v[112:113]
	v_or_b32_e32 v112, 55, v2
	v_ashrrev_i32_e32 v113, 31, v112
	v_lshlrev_b64 v[112:113], 7, v[112:113]
	v_lshl_add_u64 v[126:127], v[4:5], 0, v[112:113]
	global_load_dword v112, v[120:121], off
	global_load_dword v113, v[120:121], off offset:64
	global_load_dword v114, v[122:123], off
	global_load_dword v115, v[122:123], off offset:64
	global_load_dword v116, v[124:125], off
	global_load_dword v117, v[124:125], off offset:64
	global_load_dword v118, v[126:127], off
	global_load_dword v119, v[126:127], off offset:64
	v_or_b32_e32 v120, 56, v2
	v_ashrrev_i32_e32 v121, 31, v120
	v_lshlrev_b64 v[120:121], 7, v[120:121]
	v_lshl_add_u64 v[122:123], v[4:5], 0, v[120:121]
	v_or_b32_e32 v120, 57, v2
	v_ashrrev_i32_e32 v121, 31, v120
	v_lshlrev_b64 v[120:121], 7, v[120:121]
	v_lshl_add_u64 v[124:125], v[4:5], 0, v[120:121]
	v_or_b32_e32 v120, 58, v2
	v_ashrrev_i32_e32 v121, 31, v120
	v_lshlrev_b64 v[120:121], 7, v[120:121]
	v_lshl_add_u64 v[126:127], v[4:5], 0, v[120:121]
	v_or_b32_e32 v120, 59, v2
	v_ashrrev_i32_e32 v121, 31, v120
	v_lshlrev_b64 v[120:121], 7, v[120:121]
	v_lshl_add_u64 v[128:129], v[4:5], 0, v[120:121]
	global_load_dword v120, v[122:123], off
	global_load_dword v121, v[122:123], off offset:64
	s_nop 0
	global_load_dword v122, v[124:125], off
	global_load_dword v123, v[124:125], off offset:64
	s_nop 0
	global_load_dword v124, v[126:127], off
	global_load_dword v125, v[126:127], off offset:64
	s_nop 0
	global_load_dword v126, v[128:129], off
	global_load_dword v127, v[128:129], off offset:64
	v_or_b32_e32 v128, 60, v2
	v_ashrrev_i32_e32 v129, 31, v128
	v_lshlrev_b64 v[128:129], 7, v[128:129]
	v_lshl_add_u64 v[130:131], v[4:5], 0, v[128:129]
	v_or_b32_e32 v128, 61, v2
	v_ashrrev_i32_e32 v129, 31, v128
	v_lshlrev_b64 v[128:129], 7, v[128:129]
	v_lshl_add_u64 v[132:133], v[4:5], 0, v[128:129]
	v_or_b32_e32 v128, 62, v2
	v_ashrrev_i32_e32 v129, 31, v128
	v_or_b32_e32 v2, 63, v2
	v_lshlrev_b64 v[128:129], 7, v[128:129]
	v_ashrrev_i32_e32 v3, 31, v2
	v_lshl_add_u64 v[134:135], v[4:5], 0, v[128:129]
	v_lshlrev_b64 v[2:3], 7, v[2:3]
	v_lshl_add_u64 v[2:3], v[4:5], 0, v[2:3]
	global_load_dword v128, v[130:131], off
	global_load_dword v129, v[130:131], off offset:64
	s_nop 0
	global_load_dword v130, v[132:133], off
	global_load_dword v131, v[132:133], off offset:64
	s_nop 0
	global_load_dword v132, v[134:135], off
	global_load_dword v133, v[134:135], off offset:64
	s_nop 0
	global_load_dword v134, v[2:3], off
	global_load_dword v135, v[2:3], off offset:64
	v_readlane_b32 s2, v254, 21
	v_readlane_b32 s3, v254, 22
	v_readlane_b32 s1, v254, 20
	v_cmp_gt_i32_e64 s[2:3], 32, v200
	v_lshl_add_u32 v201, v200, 2, 0
	v_readlane_b32 s4, v254, 23
	v_readlane_b32 s5, v254, 24
	v_readlane_b32 s6, v254, 25
	v_readlane_b32 s7, v254, 26
	v_readlane_b32 s8, v254, 27
	v_readlane_b32 s9, v254, 28
	v_readlane_b32 s10, v254, 29
	v_readlane_b32 s11, v254, 30
	v_readlane_b32 s14, v254, 33
	v_readlane_b32 s15, v254, 34
	s_and_saveexec_b64 s[0:1], s[2:3]
	v_add_u32_e32 v0, 0x18410, v201
	ds_write_b32 v0, v1
	s_or_b64 exec, exec, s[0:1]
	v_cmp_eq_u32_e32 vcc, 32, v200
	s_and_saveexec_b64 s[0:1], vcc
	s_add_i32 s4, 0, 0x19510
	v_mov_b32_e32 v0, 0
	v_mov_b32_e32 v1, s4
	ds_write_b32 v1, v0
	s_or_b64 exec, exec, s[0:1]
	s_cmpk_gt_i32 s97, 0x3ff
	s_waitcnt lgkmcnt(0)
	s_barrier
	s_cbranch_scc1 .LBB0_1339
; template <bool DRY = false>
; DI void phase_ln_router(const Params& p, char* smem, int bid, int nb) {
;     ...
;   u32x2 za[8];
;   {
;     const int tf = bid * 8 + wv;
;     const bf16_t* zr = p.z1b + (size_t)(tf < NTOK ? tf : 0) * DM;
; #pragma unroll
;     for (int i = 0; i < 8; ++i) za[i] = *(const u32x2*)(zr + (i * 64 + lane) * 4);
;   }
;     ...
;       for (int i = 0; i < 8; ++i) {
;         const int c = (i * 64 + lane) * 4;
;         const float4 gg = *(const float4*)(p.ln_mix_g + c);
;         const float4 bb = *(const float4*)(p.ln_mix_b + c);
	v_ashrrev_i32_e32 v203, 6, v200
	v_add_u32_e32 v0, s38, v203
	s_movk_i32 s26, 0x2000
	v_cmp_gt_i32_e32 vcc, s26, v0
	v_and_b32_e32 v202, 63, v6
	v_lshlrev_b32_e32 v4, 3, v202
	v_cndmask_b32_e32 v2, 0, v0, vcc
	v_ashrrev_i32_e32 v3, 31, v2
	v_lshlrev_b64 v[2:3], 12, v[2:3]
	v_lshl_add_u64 v[2:3], s[56:57], 0, v[2:3]
	v_mov_b32_e32 v5, 0
	v_lshl_add_u64 v[2:3], v[2:3], 0, v[4:5]
	global_load_dwordx2 v[172:173], v[2:3], off offset:3584
	global_load_dwordx2 v[176:177], v[2:3], off offset:3072
	global_load_dwordx2 v[178:179], v[2:3], off offset:2560
	global_load_dwordx2 v[180:181], v[2:3], off offset:2048
	global_load_dwordx2 v[166:167], v[2:3], off offset:1536
	global_load_dwordx2 v[168:169], v[2:3], off offset:1024
	global_load_dwordx2 v[170:171], v[2:3], off offset:512
	global_load_dwordx2 v[174:175], v[2:3], off
	v_mbcnt_lo_u32_b32 v1, -1, 0
	v_mbcnt_hi_u32_b32 v1, -1, v1
	v_and_b32_e32 v2, 64, v1
	v_add_u32_e32 v2, 64, v2
	v_xor_b32_e32 v3, 32, v1
	v_cmp_lt_i32_e32 vcc, v3, v2
	v_lshlrev_b32_e32 v161, 2, v202
	s_add_i32 s1, 0, 0x18010
	v_cndmask_b32_e32 v3, v1, v3, vcc
	v_lshlrev_b32_e32 v204, 2, v3
	v_xor_b32_e32 v3, 16, v1
	v_cmp_lt_i32_e32 vcc, v3, v2
	v_add_u32_e32 v182, s1, v161
	v_lshl_add_u32 v212, v200, 2, s1
	v_cndmask_b32_e32 v3, v1, v3, vcc
	v_lshlrev_b32_e32 v205, 2, v3
	v_xor_b32_e32 v3, 8, v1
	v_cmp_lt_i32_e32 vcc, v3, v2
	v_lshlrev_b32_e32 v160, 16, v202
	s_lshl_b32 s1, s97, 21
	v_cndmask_b32_e32 v3, v1, v3, vcc
	v_lshlrev_b32_e32 v206, 2, v3
	v_xor_b32_e32 v3, 4, v1
	v_cmp_lt_i32_e32 vcc, v3, v2
	s_add_i32 s6, 0, 0x10010
	v_readlane_b32 s8, v254, 19
	v_cndmask_b32_e32 v3, v1, v3, vcc
	v_lshlrev_b32_e32 v207, 2, v3
	v_xor_b32_e32 v3, 2, v1
	v_cmp_lt_i32_e32 vcc, v3, v2
	v_readlane_b32 s22, v254, 33
	v_readlane_b32 s23, v254, 34
	v_cndmask_b32_e32 v3, v1, v3, vcc
	v_lshlrev_b32_e32 v208, 2, v3
	v_xor_b32_e32 v3, 1, v1
	v_cmp_lt_i32_e32 vcc, v3, v2
	v_and_b32_e32 v2, 0x3fffffe0, v200
	s_lshl_b32 s0, s96, 3
	v_cndmask_b32_e32 v1, v1, v3, vcc
	v_lshlrev_b32_e32 v209, 2, v1
	v_lshlrev_b32_e32 v1, 13, v203
	v_lshlrev_b32_e32 v3, 2, v2
	v_lshlrev_b32_e32 v2, 2, v6
	v_lshlrev_b32_e32 v6, 4, v202
	v_add3_u32 v213, 0, v1, v6
	v_lshlrev_b32_e32 v1, 18, v203
	v_and_b32_e32 v2, 0x7c, v2
	v_add3_u32 v214, s1, v1, v160
	s_lshl_b32 s1, s97, 5
	v_lshlrev_b32_e32 v1, 2, v203
	v_add3_u32 v211, s6, v3, v2
	v_mov_b32_e32 v3, v5
	v_add3_u32 v160, s1, v1, v202
	v_ashrrev_i32_e32 v1, 31, v0
	v_lshl_add_u32 v210, v7, 8, 0
	v_lshlrev_b32_e32 v184, 10, v7
	v_mov_b32_e32 v7, v5
	v_readlane_b32 s16, v254, 27
	v_readlane_b32 s17, v254, 28
	v_readlane_b32 s18, v254, 29
	v_readlane_b32 s19, v254, 30
	v_lshl_add_u64 v[156:157], s[22:23], 0, v[2:3]
	v_lshlrev_b64 v[2:3], 11, v[0:1]
	v_lshlrev_b64 v[0:1], 12, v[0:1]
	v_lshl_add_u32 v183, v136, 2, s6
	s_movk_i32 s4, 0x100
	v_lshlrev_b32_e32 v185, 7, v203
	v_lshl_add_u64 v[136:137], s[16:17], 0, v[6:7]
	v_lshl_add_u64 v[138:139], s[18:19], 0, v[6:7]
	v_or_b32_e32 v142, 0x1000, v6
	v_mov_b32_e32 v143, v5
	v_or_b32_e32 v146, 0x1400, v6
	v_mov_b32_e32 v147, v5
	v_or_b32_e32 v150, 0x1800, v6
	v_mov_b32_e32 v151, v5
	v_or_b32_e32 v6, 0x1c00, v6
	v_or_b32_e32 v2, v2, v161
	s_ashr_i32 s1, s0, 31
	v_or_b32_e32 v0, v0, v4
	v_cmp_gt_i32_e64 s[4:5], s4, v200
	v_cmp_gt_u32_e64 s[6:7], 32, v202
	v_cmp_gt_u32_e64 s[36:37], 4, v202
	v_cmp_eq_u32_e64 s[44:45], 0, v202
	v_cmp_eq_u32_e64 s[46:47], 1, v202
	v_cmp_eq_u32_e64 s[48:49], 2, v202
	v_lshl_add_u64 v[140:141], s[16:17], 0, v[142:143]
	v_lshl_add_u64 v[142:143], s[18:19], 0, v[142:143]
	v_lshl_add_u64 v[144:145], s[16:17], 0, v[146:147]
	v_lshl_add_u64 v[146:147], s[18:19], 0, v[146:147]
	v_lshl_add_u64 v[148:149], s[16:17], 0, v[150:151]
	v_lshl_add_u64 v[150:151], s[18:19], 0, v[150:151]
	v_lshl_add_u64 v[152:153], s[16:17], 0, v[6:7]
	v_lshl_add_u64 v[154:155], s[18:19], 0, v[6:7]
	v_lshlrev_b32_e32 v222, 4, v200
	global_load_dwordx4 v[224:227], v222, s[16:17]
	global_load_dwordx4 v[228:231], v222, s[18:19]
	v_add_u32_e32 v223, 0x1c000, v222
	v_and_b32_e32 v136, 63, v200
	v_lshlrev_b32_e32 v136, 4, v136
	v_add_u32_e32 v136, 0x1c000, v136
	s_waitcnt vmcnt(0)
	ds_write_b128 v223, v[224:227]
	ds_write_b128 v223, v[228:231] offset:8192
	s_waitcnt lgkmcnt(0)
	s_barrier
	v_lshl_add_u64 v[158:159], s[56:57], 0, v[4:5]
	s_lshl_b32 s27, s96, 21
	s_lshl_b32 s28, s96, 5
	v_add_u32_e32 v215, s0, v203
	v_lshl_add_u64 v[162:163], s[68:69], 0, v[2:3]
	s_lshl_b64 s[16:17], s[0:1], 11
	v_lshl_add_u64 v[164:165], s[88:89], 0, v[0:1]
	s_lshl_b64 s[18:19], s[0:1], 12
	v_mov_b32_e32 v216, 0x3727c5ac
	s_mov_b32 s1, 0x800000
	s_mov_b32 s29, 0xc3dc0000
	v_add_u32_e32 v217, v183, v184
	v_add_u32_e32 v218, v182, v185
	v_mov_b32_e32 v219, 1
	s_add_i32 s30, 0, 0x19510
	s_movk_i32 s31, 0x400
	v_mov_b32_e32 v220, 0x43dc0000
	v_mov_b32_e32 v221, 0xff61b1e6
	s_mov_b32 s33, s38
	v_readlane_b32 s9, v254, 20
	v_readlane_b32 s10, v254, 21
	v_readlane_b32 s11, v254, 22
	v_readlane_b32 s12, v254, 23
	v_readlane_b32 s13, v254, 24
	v_readlane_b32 s14, v254, 25
	v_readlane_b32 s15, v254, 26
	v_readlane_b32 s20, v254, 31
	v_readlane_b32 s21, v254, 32
	s_branch .LBB0_1330

; DI float bflo(unsigned u) { return __uint_as_float(u << 16); }
; DI float bfhi(unsigned u) { return __uint_as_float(u & 0xffff0000u); }
; template <bool DRY = false>
; DI void phase_ln_router(const Params& p, char* smem, int bid, int nb) {
;     ...
;     {
;       float v[32];
; #pragma unroll
;       for (int i = 0; i < 8; ++i) {
;         const u32x2 a = za[i];
;         v[4 * i] = bflo(a.x); v[4 * i + 1] = bfhi(a.x); v[4 * i + 2] = bflo(a.y); v[4 * i + 3] = bfhi(a.y);
;       }
;       {
;         const int tn2 = t + nb * 8;
;         const bf16_t* zr = p.z1b + (size_t)(tn2 < NTOK ? tn2 : t) * DM;
; #pragma unroll
;         for (int i = 0; i < 8; ++i) za[i] = *(const u32x2*)(zr + (i * 64 + lane) * 4);
;       }
;       float s = 0.f;
; #pragma unroll
;       for (int i = 0; i < 32; ++i) s += v[i];
;       s = wave_sum(s);
;       const float mu = s * (1.f / 2048.f);
;       float q = 0.f;
; #pragma unroll
;       for (int i = 0; i < 32; ++i) { const float d = v[i] - mu; q += d * d; }
;       q = wave_sum(q);
;       const float rs = rsqrtf(q * (1.f / 2048.f) + LN_EPS);
; #pragma unroll
;       for (int i = 0; i < 8; ++i) {
;         const int c = (i * 64 + lane) * 4;
;         const float4 gg = *(const float4*)(p.ln_mix_g + c);
;         const float4 bb = *(const float4*)(p.ln_mix_b + c);
.LBB0_1330:
	s_waitcnt vmcnt(0)
	v_lshlrev_b32_e32 v182, 16, v174
	v_and_b32_e32 v183, 0xffff0000, v174
	v_add_f32_e32 v0, 0, v182
	v_add_f32_e32 v0, v0, v183
	v_lshlrev_b32_e32 v174, 16, v175
	v_and_b32_e32 v175, 0xffff0000, v175
	v_add_f32_e32 v0, v0, v174
	v_add_f32_e32 v0, v0, v175
	v_lshlrev_b32_e32 v184, 16, v170
	v_and_b32_e32 v185, 0xffff0000, v170
	v_add_f32_e32 v0, v0, v184
	v_add_f32_e32 v0, v0, v185
	v_lshlrev_b32_e32 v170, 16, v171
	v_and_b32_e32 v171, 0xffff0000, v171
	v_add_f32_e32 v0, v0, v170
	v_add_f32_e32 v0, v0, v171
	v_lshlrev_b32_e32 v186, 16, v168
	v_and_b32_e32 v187, 0xffff0000, v168
	v_add_f32_e32 v0, v0, v186
	v_add_f32_e32 v0, v0, v187
	v_lshlrev_b32_e32 v168, 16, v169
	v_and_b32_e32 v169, 0xffff0000, v169
	v_add_f32_e32 v0, v0, v168
	v_add_f32_e32 v0, v0, v169
	v_lshlrev_b32_e32 v188, 16, v166
	v_and_b32_e32 v189, 0xffff0000, v166
	v_add_f32_e32 v0, v0, v188
	v_add_f32_e32 v0, v0, v189
	v_lshlrev_b32_e32 v166, 16, v167
	v_and_b32_e32 v167, 0xffff0000, v167
	v_add_f32_e32 v0, v0, v166
	v_add_f32_e32 v0, v0, v167
	v_lshlrev_b32_e32 v190, 16, v180
	v_and_b32_e32 v191, 0xffff0000, v180
	v_add_f32_e32 v0, v0, v190
	v_add_f32_e32 v0, v0, v191
	v_lshlrev_b32_e32 v180, 16, v181
	v_and_b32_e32 v181, 0xffff0000, v181
	v_add_f32_e32 v0, v0, v180
	v_add_f32_e32 v0, v0, v181
	v_lshlrev_b32_e32 v192, 16, v178
	v_and_b32_e32 v193, 0xffff0000, v178
	v_add_f32_e32 v0, v0, v192
	v_add_f32_e32 v0, v0, v193
	v_lshlrev_b32_e32 v178, 16, v179
	v_and_b32_e32 v179, 0xffff0000, v179
	v_add_f32_e32 v0, v0, v178
	v_add_f32_e32 v0, v0, v179
	v_lshlrev_b32_e32 v222, 16, v176
	v_and_b32_e32 v223, 0xffff0000, v176
	v_add_f32_e32 v0, v0, v222
	v_add_f32_e32 v0, v0, v223
	v_lshlrev_b32_e32 v176, 16, v177
	v_and_b32_e32 v177, 0xffff0000, v177
	v_add_f32_e32 v0, v0, v176
	v_add_f32_e32 v0, v0, v177
	v_lshlrev_b32_e32 v224, 16, v172
	v_and_b32_e32 v225, 0xffff0000, v172
	v_add_f32_e32 v0, v0, v224
	v_add_f32_e32 v0, v0, v225
	v_lshlrev_b32_e32 v172, 16, v173
	v_and_b32_e32 v173, 0xffff0000, v173
	v_add_f32_e32 v0, v0, v172
	v_add_f32_e32 v0, v0, v173
	ds_bpermute_b32 v1, v204, v0
	s_waitcnt lgkmcnt(0)
	v_add_f32_e32 v0, v0, v1
	ds_bpermute_b32 v1, v205, v0
	s_waitcnt lgkmcnt(0)
	v_add_f32_e32 v0, v0, v1
	ds_bpermute_b32 v1, v206, v0
	s_waitcnt lgkmcnt(0)
	v_add_f32_e32 v0, v0, v1
	ds_bpermute_b32 v1, v207, v0
	s_waitcnt lgkmcnt(0)
	v_add_f32_e32 v0, v0, v1
	ds_bpermute_b32 v1, v208, v0
	s_waitcnt lgkmcnt(0)
	v_add_f32_e32 v161, v0, v1
	ds_bpermute_b32 v194, v209, v161
	ds_read_b128 v[0:3], v136
	ds_read_b128 v[4:7], v136 offset:8192
	s_waitcnt lgkmcnt(0)
	v_add_f32_e32 v161, v161, v194
	v_mul_f32_e32 v226, 0x3a000000, v161
	v_pk_add_f32 v[228:229], v[182:183], v[226:227] op_sel_hi:[1,0] neg_lo:[0,1] neg_hi:[0,1]
	v_pk_add_f32 v[232:233], v[174:175], v[226:227] op_sel_hi:[1,0] neg_lo:[0,1] neg_hi:[0,1]
	v_pk_mul_f32 v[230:231], v[228:229], v[228:229]
	v_pk_mul_f32 v[174:175], v[232:233], v[232:233]
	v_add_f32_e32 v161, v230, v231
	v_pk_add_f32 v[234:235], v[184:185], v[226:227] op_sel_hi:[1,0] neg_lo:[0,1] neg_hi:[0,1]
	v_add_f32_e32 v161, v174, v161
	v_pk_mul_f32 v[236:237], v[234:235], v[234:235]
	v_add_f32_e32 v161, v175, v161
	v_pk_add_f32 v[238:239], v[170:171], v[226:227] op_sel_hi:[1,0] neg_lo:[0,1] neg_hi:[0,1]
	v_add_f32_e32 v161, v236, v161
	v_pk_mul_f32 v[170:171], v[238:239], v[238:239]
	v_add_f32_e32 v161, v237, v161
	v_pk_add_f32 v[240:241], v[186:187], v[226:227] op_sel_hi:[1,0] neg_lo:[0,1] neg_hi:[0,1]
	v_add_f32_e32 v161, v170, v161
	v_pk_mul_f32 v[242:243], v[240:241], v[240:241]
	v_add_f32_e32 v161, v171, v161
	v_pk_add_f32 v[244:245], v[168:169], v[226:227] op_sel_hi:[1,0] neg_lo:[0,1] neg_hi:[0,1]
	v_add_f32_e32 v161, v242, v161
	v_pk_mul_f32 v[168:169], v[244:245], v[244:245]
	v_add_f32_e32 v161, v243, v161
	v_pk_add_f32 v[246:247], v[188:189], v[226:227] op_sel_hi:[1,0] neg_lo:[0,1] neg_hi:[0,1]
	v_add_f32_e32 v161, v168, v161
	v_pk_mul_f32 v[248:249], v[246:247], v[246:247]
	v_add_f32_e32 v161, v169, v161
	v_pk_add_f32 v[250:251], v[166:167], v[226:227] op_sel_hi:[1,0] neg_lo:[0,1] neg_hi:[0,1]
	v_add_f32_e32 v161, v248, v161
	v_pk_mul_f32 v[166:167], v[250:251], v[250:251]
	v_add_f32_e32 v161, v249, v161
	v_pk_add_f32 v[196:197], v[190:191], v[226:227] op_sel_hi:[1,0] neg_lo:[0,1] neg_hi:[0,1]
	v_add_f32_e32 v161, v166, v161
	v_pk_mul_f32 v[190:191], v[196:197], v[196:197]
	v_add_f32_e32 v161, v167, v161
	v_pk_add_f32 v[198:199], v[180:181], v[226:227] op_sel_hi:[1,0] neg_lo:[0,1] neg_hi:[0,1]
	v_add_f32_e32 v161, v190, v161
	v_pk_mul_f32 v[180:181], v[198:199], v[198:199]
	v_add_f32_e32 v161, v191, v161
	v_pk_add_f32 v[192:193], v[192:193], v[226:227] op_sel_hi:[1,0] neg_lo:[0,1] neg_hi:[0,1]
	v_add_f32_e32 v161, v180, v161
	v_pk_mul_f32 v[252:253], v[192:193], v[192:193]
	v_add_f32_e32 v161, v181, v161
	v_pk_add_f32 v[194:195], v[178:179], v[226:227] op_sel_hi:[1,0] neg_lo:[0,1] neg_hi:[0,1]
	v_add_f32_e32 v161, v252, v161
	v_pk_mul_f32 v[178:179], v[194:195], v[194:195]
	v_add_f32_e32 v161, v253, v161
	v_pk_add_f32 v[186:187], v[222:223], v[226:227] op_sel_hi:[1,0] neg_lo:[0,1] neg_hi:[0,1]
	v_add_f32_e32 v161, v178, v161
	v_pk_mul_f32 v[222:223], v[186:187], v[186:187]
	v_add_f32_e32 v161, v179, v161
	v_pk_add_f32 v[188:189], v[176:177], v[226:227] op_sel_hi:[1,0] neg_lo:[0,1] neg_hi:[0,1]
	v_add_f32_e32 v161, v222, v161
	v_pk_mul_f32 v[176:177], v[188:189], v[188:189]
	v_add_f32_e32 v161, v223, v161
	v_pk_add_f32 v[182:183], v[224:225], v[226:227] op_sel_hi:[1,0] neg_lo:[0,1] neg_hi:[0,1]
	v_add_f32_e32 v161, v176, v161
	v_pk_mul_f32 v[224:225], v[182:183], v[182:183]
	v_add_f32_e32 v161, v177, v161
	v_pk_add_f32 v[184:185], v[172:173], v[226:227] op_sel_hi:[1,0] neg_lo:[0,1] neg_hi:[0,1]
	v_add_f32_e32 v161, v224, v161
	v_pk_mul_f32 v[172:173], v[184:185], v[184:185]
	v_add_f32_e32 v161, v225, v161
	v_add_f32_e32 v161, v172, v161
	v_add_f32_e32 v161, v173, v161
	ds_bpermute_b32 v166, v204, v161
	v_add_u32_e32 v168, s33, v215
	v_add_u32_e32 v167, s33, v203
	v_cmp_gt_i32_e32 vcc, s26, v168
	s_waitcnt lgkmcnt(0)
; template <bool DRY = false>
; DI void phase_ln_router(const Params& p, char* smem, int bid, int nb) {
;     ...
;       {
;         const int tn2 = t + nb * 8;
;         const bf16_t* zr = p.z1b + (size_t)(tn2 < NTOK ? tn2 : t) * DM;
; #pragma unroll
;         for (int i = 0; i < 8; ++i) za[i] = *(const u32x2*)(zr + (i * 64 + lane) * 4);
;       }
;       float s = 0.f;
; #pragma unroll
;       for (int i = 0; i < 32; ++i) s += v[i];
;       s = wave_sum(s);
;       const float mu = s * (1.f / 2048.f);
;       float q = 0.f;
; #pragma unroll
;       for (int i = 0; i < 32; ++i) { const float d = v[i] - mu; q += d * d; }
;       q = wave_sum(q);
;       const float rs = rsqrtf(q * (1.f / 2048.f) + LN_EPS);
; #pragma unroll
;       for (int i = 0; i < 8; ++i) {
;         const int c = (i * 64 + lane) * 4;
;         const float4 gg = *(const float4*)(p.ln_mix_g + c);
;         const float4 bb = *(const float4*)(p.ln_mix_b + c);
;         float4 o;
;         o.x = (v[4 * i + 0] - mu) * rs * gg.x + bb.x;
;         o.y = (v[4 * i + 1] - mu) * rs * gg.y + bb.y;
;         o.z = (v[4 * i + 2] - mu) * rs * gg.z + bb.z;
;         o.w = (v[4 * i + 3] - mu) * rs * gg.w + bb.w;
;         { uint2 pk; pk.x = pack2(o.x, o.y); pk.y = pack2(o.z, o.w); *(uint2*)(p.h1b + (size_t)t * DM + c) = pk; }
;     ...
;         {
;           int pq = 0;
;           pq = __builtin_amdgcn_cvt_pk_fp8_f32(fminf(fmaxf(o.x * 16.f, -440.f), 440.f), fminf(fmaxf(o.y * 16.f, -440.f), 440.f), pq, false);
;           pq = __builtin_amdgcn_cvt_pk_fp8_f32(fminf(fmaxf(o.z * 16.f, -440.f), 440.f), fminf(fmaxf(o.w * 16.f, -440.f), 440.f), pq, true);
;           *(int*)(p.h1q + (size_t)t * DM + c) = pq;
;         }
	v_add_f32_e32 v161, v161, v166
	ds_bpermute_b32 v166, v205, v161
	s_waitcnt lgkmcnt(0)
	v_add_f32_e32 v161, v161, v166
	ds_bpermute_b32 v166, v206, v161
	s_waitcnt lgkmcnt(0)
	v_add_f32_e32 v161, v161, v166
	ds_bpermute_b32 v166, v207, v161
	s_waitcnt lgkmcnt(0)
	v_add_f32_e32 v161, v161, v166
	ds_bpermute_b32 v169, v208, v161
	v_cndmask_b32_e32 v166, v167, v168, vcc
	v_ashrrev_i32_e32 v167, 31, v166
	v_lshlrev_b64 v[166:167], 12, v[166:167]
	v_lshl_add_u64 v[172:173], v[158:159], 0, v[166:167]
	s_waitcnt lgkmcnt(0)
	v_add_f32_e32 v161, v161, v169
	ds_bpermute_b32 v176, v209, v161
	global_load_dwordx2 v[174:175], v[172:173], off
	global_load_dwordx2 v[170:171], v[172:173], off offset:512
	global_load_dwordx2 v[168:169], v[172:173], off offset:1024
	global_load_dwordx2 v[166:167], v[172:173], off offset:1536
	s_waitcnt lgkmcnt(0)
	v_add_f32_e32 v161, v161, v176
	v_fmamk_f32 v161, v161, 0x3a000000, v216
	v_mul_f32_e32 v176, 0x4b800000, v161
	v_cmp_gt_f32_e32 vcc, s1, v161
	s_nop 1
	v_cndmask_b32_e32 v161, v161, v176, vcc
	v_rsq_f32_e32 v161, v161
	global_load_dwordx2 v[180:181], v[172:173], off offset:2048
	global_load_dwordx2 v[178:179], v[172:173], off offset:2560
	global_load_dwordx2 v[176:177], v[172:173], off offset:3072
	s_nop 0
	global_load_dwordx2 v[172:173], v[172:173], off offset:3584
	v_mul_f32_e32 v190, 0x45800000, v161
	v_cndmask_b32_e32 v190, v161, v190, vcc
	v_pk_mul_f32 v[222:223], v[228:229], v[190:191] op_sel_hi:[1,0]
	v_pk_mul_f32 v[226:227], v[234:235], v[190:191] op_sel_hi:[1,0]
	s_waitcnt vmcnt(8)
	v_pk_fma_f32 v[0:1], v[0:1], v[222:223], v[4:5]
	v_pk_mul_f32 v[4:5], v[232:233], v[190:191] op_sel_hi:[1,0]
	v_pk_mul_f32 v[228:229], v[238:239], v[190:191] op_sel_hi:[1,0]
	v_pk_fma_f32 v[2:3], v[2:3], v[4:5], v[6:7]
	v_mul_f32_e32 v4, 0x41800000, v0
	v_mul_f32_e32 v5, 0x41800000, v1
	v_med3_f32 v4, v4, s29, v220
	v_med3_f32 v5, v5, s29, v220
	v_mov_b32_e32 v6, 0
	v_cvt_pk_fp8_f32 v6, v4, v5
	v_mul_f32_e32 v4, 0x41800000, v2
	v_mul_f32_e32 v5, 0x41800000, v3
	v_med3_f32 v4, v4, s29, v220
	v_med3_f32 v5, v5, s29, v220
	v_cvt_pk_fp8_f32 v6, v4, v5 op_sel:[0,0,1]
	v_cvt_pk_bf16_f32 v4, v0, v1
	v_cvt_pk_bf16_f32 v5, v2, v3
	global_store_dwordx2 v[164:165], v[4:5], off
	global_store_dword v[162:163], v6, off
	ds_read_b128 v[4:7], v136 offset:1024
	s_nop 0
	ds_read_b128 v[222:225], v136 offset:9216
	v_mov_b32_e32 v161, 0
	s_waitcnt vmcnt(0) lgkmcnt(0)
	v_pk_fma_f32 v[4:5], v[4:5], v[226:227], v[222:223]
	s_nop 0
	v_mul_f32_e32 v191, 0x41800000, v4
	v_mul_f32_e32 v222, 0x41800000, v5
	v_med3_f32 v191, v191, s29, v220
	v_med3_f32 v222, v222, s29, v220
	v_cvt_pk_fp8_f32 v161, v191, v222
	v_pk_fma_f32 v[6:7], v[6:7], v[228:229], v[224:225]
	s_nop 0
	v_mul_f32_e32 v223, 0x41800000, v6
	v_mul_f32_e32 v191, 0x41800000, v7
	v_med3_f32 v222, v223, s29, v220
	v_med3_f32 v191, v191, s29, v220
	v_cvt_pk_fp8_f32 v161, v222, v191 op_sel:[0,0,1]
	v_cvt_pk_bf16_f32 v222, v4, v5
	v_cvt_pk_bf16_f32 v223, v6, v7
	global_store_dwordx2 v[164:165], v[222:223], off offset:512
	global_store_dword v[162:163], v161, off offset:256
	ds_read_b128 v[222:225], v136 offset:2048
	s_nop 0
	ds_read_b128 v[226:229], v136 offset:10240
	v_pk_mul_f32 v[230:231], v[240:241], v[190:191] op_sel_hi:[1,0]
	v_pk_mul_f32 v[232:233], v[244:245], v[190:191] op_sel_hi:[1,0]
	v_mov_b32_e32 v161, 0
	s_waitcnt lgkmcnt(0)
	v_pk_fma_f32 v[222:223], v[222:223], v[230:231], v[226:227]
	s_nop 0
	v_mul_f32_e32 v191, 0x41800000, v222
	v_mul_f32_e32 v226, 0x41800000, v223
	v_med3_f32 v191, v191, s29, v220
	v_med3_f32 v226, v226, s29, v220
	v_cvt_pk_fp8_f32 v161, v191, v226
	v_pk_fma_f32 v[224:225], v[224:225], v[232:233], v[228:229]
	s_nop 0
	v_mul_f32_e32 v227, 0x41800000, v224
	v_mul_f32_e32 v191, 0x41800000, v225
	v_med3_f32 v226, v227, s29, v220
	v_med3_f32 v191, v191, s29, v220
	v_cvt_pk_fp8_f32 v161, v226, v191 op_sel:[0,0,1]
	v_cvt_pk_bf16_f32 v226, v222, v223
	v_cvt_pk_bf16_f32 v227, v224, v225
	global_store_dwordx2 v[164:165], v[226:227], off offset:1024
	global_store_dword v[162:163], v161, off offset:512
	ds_read_b128 v[226:229], v136 offset:3072
	s_nop 0
	ds_read_b128 v[230:233], v136 offset:11264
	v_pk_mul_f32 v[234:235], v[246:247], v[190:191] op_sel_hi:[1,0]
	v_pk_mul_f32 v[236:237], v[250:251], v[190:191] op_sel_hi:[1,0]
	v_mov_b32_e32 v161, 0
	s_waitcnt lgkmcnt(0)
	v_pk_fma_f32 v[226:227], v[226:227], v[234:235], v[230:231]
	s_nop 0
	v_mul_f32_e32 v191, 0x41800000, v226
	v_mul_f32_e32 v230, 0x41800000, v227
	v_med3_f32 v191, v191, s29, v220
	v_med3_f32 v230, v230, s29, v220
	v_cvt_pk_fp8_f32 v161, v191, v230
	v_pk_fma_f32 v[228:229], v[228:229], v[236:237], v[232:233]
	s_nop 0
	v_mul_f32_e32 v231, 0x41800000, v228
	v_mul_f32_e32 v191, 0x41800000, v229
	v_med3_f32 v230, v231, s29, v220
	v_med3_f32 v191, v191, s29, v220
	v_cvt_pk_fp8_f32 v161, v230, v191 op_sel:[0,0,1]
	v_cvt_pk_bf16_f32 v230, v226, v227
	v_cvt_pk_bf16_f32 v231, v228, v229
	global_store_dwordx2 v[164:165], v[230:231], off offset:1536
	global_store_dword v[162:163], v161, off offset:768
	ds_read_b128 v[230:233], v136 offset:4096
	s_nop 0
	ds_read_b128 v[234:237], v136 offset:12288
	v_pk_mul_f32 v[196:197], v[196:197], v[190:191] op_sel_hi:[1,0]
	v_pk_mul_f32 v[198:199], v[198:199], v[190:191] op_sel_hi:[1,0]
	v_mov_b32_e32 v161, 0
	s_waitcnt lgkmcnt(0)
; template <bool DRY = false>
; DI void phase_ln_router(const Params& p, char* smem, int bid, int nb) {
;     ...
;       for (int i = 0; i < 8; ++i) {
;         const int c = (i * 64 + lane) * 4;
;         const float4 gg = *(const float4*)(p.ln_mix_g + c);
;         const float4 bb = *(const float4*)(p.ln_mix_b + c);
;         float4 o;
;         o.x = (v[4 * i + 0] - mu) * rs * gg.x + bb.x;
;         o.y = (v[4 * i + 1] - mu) * rs * gg.y + bb.y;
;         o.z = (v[4 * i + 2] - mu) * rs * gg.z + bb.z;
;         o.w = (v[4 * i + 3] - mu) * rs * gg.w + bb.w;
;         { uint2 pk; pk.x = pack2(o.x, o.y); pk.y = pack2(o.z, o.w); *(uint2*)(p.h1b + (size_t)t * DM + c) = pk; }
;     ...
;         {
;           int pq = 0;
;           pq = __builtin_amdgcn_cvt_pk_fp8_f32(fminf(fmaxf(o.x * 16.f, -440.f), 440.f), fminf(fmaxf(o.y * 16.f, -440.f), 440.f), pq, false);
;           pq = __builtin_amdgcn_cvt_pk_fp8_f32(fminf(fmaxf(o.z * 16.f, -440.f), 440.f), fminf(fmaxf(o.w * 16.f, -440.f), 440.f), pq, true);
;           *(int*)(p.h1q + (size_t)t * DM + c) = pq;
;         }
;     ...
;         *(float4*)(hs + wv * 2048 + c) = o;
;       }
;     }
;     __syncthreads();
;     {
;       f32x2_t acc[8];
; #pragma unroll
;       for (int j = 0; j < 8; ++j) acc[j] = (f32x2_t){0.f, 0.f};
; #pragma unroll
;       for (int j = 0; j < 8; ++j) {
; #pragma unroll
;         for (int i4 = 0; i4 < 16; ++i4) {
;           const float4 h = *(const float4*)(hs + j * 2048 + ks * 64 + 4 * i4);
;           acc[j] = __builtin_elementwise_fma((f32x2_t){h.x, h.x}, wr[4 * i4], acc[j]); acc[j] = __builtin_elementwise_fma((f32x2_t){h.y, h.y}, wr[4 * i4 + 1], acc[j]);
;           acc[j] = __builtin_elementwise_fma((f32x2_t){h.z, h.z}, wr[4 * i4 + 2], acc[j]); acc[j] = __builtin_elementwise_fma((f32x2_t){h.w, h.w}, wr[4 * i4 + 3], acc[j]);
	v_pk_fma_f32 v[196:197], v[196:197], v[230:231], v[234:235]
	s_nop 0
	v_mul_f32_e32 v191, 0x41800000, v196
	v_mul_f32_e32 v230, 0x41800000, v197
	v_med3_f32 v191, v191, s29, v220
	v_med3_f32 v230, v230, s29, v220
	v_cvt_pk_fp8_f32 v161, v191, v230
	v_pk_fma_f32 v[198:199], v[198:199], v[232:233], v[236:237]
	s_nop 0
	v_mul_f32_e32 v231, 0x41800000, v198
	v_mul_f32_e32 v191, 0x41800000, v199
	v_med3_f32 v230, v231, s29, v220
	v_med3_f32 v191, v191, s29, v220
	v_cvt_pk_fp8_f32 v161, v230, v191 op_sel:[0,0,1]
	v_cvt_pk_bf16_f32 v230, v196, v197
	v_cvt_pk_bf16_f32 v231, v198, v199
	global_store_dwordx2 v[164:165], v[230:231], off offset:2048
	global_store_dword v[162:163], v161, off offset:1024
	ds_read_b128 v[230:233], v136 offset:5120
	s_nop 0
	ds_read_b128 v[234:237], v136 offset:13312
	v_pk_mul_f32 v[192:193], v[192:193], v[190:191] op_sel_hi:[1,0]
	v_pk_mul_f32 v[194:195], v[194:195], v[190:191] op_sel_hi:[1,0]
	v_mov_b32_e32 v161, 0
	s_waitcnt lgkmcnt(0)
	v_pk_fma_f32 v[192:193], v[192:193], v[230:231], v[234:235]
	s_nop 0
	v_mul_f32_e32 v191, 0x41800000, v192
	v_mul_f32_e32 v230, 0x41800000, v193
	v_med3_f32 v191, v191, s29, v220
	v_med3_f32 v230, v230, s29, v220
	v_cvt_pk_fp8_f32 v161, v191, v230
	v_pk_fma_f32 v[194:195], v[194:195], v[232:233], v[236:237]
	s_nop 0
	v_mul_f32_e32 v231, 0x41800000, v194
	v_mul_f32_e32 v191, 0x41800000, v195
	v_med3_f32 v230, v231, s29, v220
	v_med3_f32 v191, v191, s29, v220
	v_cvt_pk_fp8_f32 v161, v230, v191 op_sel:[0,0,1]
	v_cvt_pk_bf16_f32 v230, v192, v193
	v_cvt_pk_bf16_f32 v231, v194, v195
	global_store_dwordx2 v[164:165], v[230:231], off offset:2560
	global_store_dword v[162:163], v161, off offset:1280
	ds_read_b128 v[230:233], v136 offset:6144
	s_nop 0
	ds_read_b128 v[234:237], v136 offset:14336
	v_pk_mul_f32 v[186:187], v[186:187], v[190:191] op_sel_hi:[1,0]
	v_pk_mul_f32 v[188:189], v[188:189], v[190:191] op_sel_hi:[1,0]
	v_mov_b32_e32 v161, 0
	s_waitcnt lgkmcnt(0)
	v_pk_fma_f32 v[186:187], v[186:187], v[230:231], v[234:235]
	s_nop 0
	v_mul_f32_e32 v191, 0x41800000, v186
	v_mul_f32_e32 v230, 0x41800000, v187
	v_med3_f32 v191, v191, s29, v220
	v_med3_f32 v230, v230, s29, v220
	v_cvt_pk_fp8_f32 v161, v191, v230
	v_pk_fma_f32 v[188:189], v[188:189], v[232:233], v[236:237]
	s_nop 0
	v_mul_f32_e32 v231, 0x41800000, v188
	v_mul_f32_e32 v191, 0x41800000, v189
	v_med3_f32 v230, v231, s29, v220
	v_med3_f32 v191, v191, s29, v220
	v_cvt_pk_fp8_f32 v161, v230, v191 op_sel:[0,0,1]
	v_cvt_pk_bf16_f32 v230, v186, v187
	v_cvt_pk_bf16_f32 v231, v188, v189
	global_store_dwordx2 v[164:165], v[230:231], off offset:3072
	global_store_dword v[162:163], v161, off offset:1536
	ds_read_b128 v[230:233], v136 offset:7168
	s_nop 0
	ds_read_b128 v[234:237], v136 offset:15360
	v_pk_mul_f32 v[182:183], v[182:183], v[190:191] op_sel_hi:[1,0]
	ds_write_b128 v213, v[0:3] offset:16
	ds_write_b128 v213, v[4:7] offset:1040
	ds_write_b128 v213, v[222:225] offset:2064
	ds_write_b128 v213, v[226:229] offset:3088
	ds_write_b128 v213, v[196:199] offset:4112
	ds_write_b128 v213, v[192:195] offset:5136
	ds_write_b128 v213, v[186:189] offset:6160
	v_mov_b32_e32 v161, 0
	v_pk_mul_f32 v[184:185], v[184:185], v[190:191] op_sel_hi:[1,0]
	s_waitcnt lgkmcnt(0)
	v_pk_fma_f32 v[0:1], v[182:183], v[230:231], v[234:235]
	s_nop 0
	v_mul_f32_e32 v5, 0x41800000, v0
	v_mul_f32_e32 v6, 0x41800000, v1
	v_med3_f32 v5, v5, s29, v220
	v_med3_f32 v6, v6, s29, v220
	v_cvt_pk_fp8_f32 v161, v5, v6
	v_pk_fma_f32 v[2:3], v[184:185], v[232:233], v[236:237]
	v_cvt_pk_bf16_f32 v4, v0, v1
	v_mul_f32_e32 v7, 0x41800000, v2
	v_mul_f32_e32 v5, 0x41800000, v3
	v_med3_f32 v6, v7, s29, v220
	v_med3_f32 v5, v5, s29, v220
	v_cvt_pk_fp8_f32 v161, v6, v5 op_sel:[0,0,1]
	v_cvt_pk_bf16_f32 v5, v2, v3
	ds_write_b128 v213, v[0:3] offset:7184
	global_store_dwordx2 v[164:165], v[4:5], off offset:3584
	global_store_dword v[162:163], v161, off offset:1792
	s_waitcnt lgkmcnt(0)
	s_barrier
	ds_read_b128 v[0:3], v210 offset:16
	ds_read_b128 v[4:7], v210 offset:32
	ds_read_b128 v[182:185], v210 offset:48
	ds_read_b128 v[186:189], v210 offset:64
	ds_read_b128 v[192:195], v210 offset:80
	ds_read_b128 v[196:199], v210 offset:96
	ds_read_b128 v[222:225], v210 offset:112
	ds_read_b128 v[226:229], v210 offset:128
	s_waitcnt lgkmcnt(7)
	v_pk_fma_f32 v[190:191], v[0:1], v[8:9], 0 op_sel_hi:[0,1,0]
	v_pk_fma_f32 v[0:1], v[0:1], v[10:11], v[190:191] op_sel:[1,0,0]
	v_mov_b32_e32 v230, v3
	v_pk_fma_f32 v[0:1], v[2:3], v[12:13], v[0:1] op_sel_hi:[0,1,1]
	v_pk_fma_f32 v[0:1], v[230:231], v[14:15], v[0:1] op_sel_hi:[0,1,1]
	s_waitcnt lgkmcnt(6)
	v_pk_fma_f32 v[0:1], v[4:5], v[16:17], v[0:1] op_sel_hi:[0,1,1]
	v_pk_fma_f32 v[0:1], v[4:5], v[18:19], v[0:1] op_sel:[1,0,0]
	v_mov_b32_e32 v232, v7
	v_pk_fma_f32 v[0:1], v[6:7], v[20:21], v[0:1] op_sel_hi:[0,1,1]
	v_pk_fma_f32 v[0:1], v[232:233], v[22:23], v[0:1] op_sel_hi:[0,1,1]
	s_waitcnt lgkmcnt(5)
	v_pk_fma_f32 v[0:1], v[182:183], v[24:25], v[0:1] op_sel_hi:[0,1,1]
	v_pk_fma_f32 v[0:1], v[182:183], v[26:27], v[0:1] op_sel:[1,0,0]
	v_mov_b32_e32 v234, v185
	v_pk_fma_f32 v[0:1], v[184:185], v[28:29], v[0:1] op_sel_hi:[0,1,1]
	v_pk_fma_f32 v[0:1], v[234:235], v[30:31], v[0:1] op_sel_hi:[0,1,1]
	s_waitcnt lgkmcnt(4)
	v_pk_fma_f32 v[0:1], v[186:187], v[32:33], v[0:1] op_sel_hi:[0,1,1]
	v_pk_fma_f32 v[0:1], v[186:187], v[34:35], v[0:1] op_sel:[1,0,0]
	v_mov_b32_e32 v236, v189
	v_pk_fma_f32 v[0:1], v[188:189], v[36:37], v[0:1] op_sel_hi:[0,1,1]
	v_pk_fma_f32 v[0:1], v[236:237], v[38:39], v[0:1] op_sel_hi:[0,1,1]
	s_waitcnt lgkmcnt(3)
; template <bool DRY = false>
; DI void phase_ln_router(const Params& p, char* smem, int bid, int nb) {
;     ...
;       f32x2_t acc[8];
; #pragma unroll
;       for (int j = 0; j < 8; ++j) acc[j] = (f32x2_t){0.f, 0.f};
; #pragma unroll
;       for (int j = 0; j < 8; ++j) {
; #pragma unroll
;         for (int i4 = 0; i4 < 16; ++i4) {
;           const float4 h = *(const float4*)(hs + j * 2048 + ks * 64 + 4 * i4);
;           acc[j] = __builtin_elementwise_fma((f32x2_t){h.x, h.x}, wr[4 * i4], acc[j]); acc[j] = __builtin_elementwise_fma((f32x2_t){h.y, h.y}, wr[4 * i4 + 1], acc[j]);
;           acc[j] = __builtin_elementwise_fma((f32x2_t){h.z, h.z}, wr[4 * i4 + 2], acc[j]); acc[j] = __builtin_elementwise_fma((f32x2_t){h.w, h.w}, wr[4 * i4 + 3], acc[j]);
;           if ((i4 & 7) == 7) __builtin_amdgcn_sched_barrier(0);
;         }
;       }
	v_pk_fma_f32 v[0:1], v[192:193], v[40:41], v[0:1] op_sel_hi:[0,1,1]
	v_pk_fma_f32 v[0:1], v[192:193], v[42:43], v[0:1] op_sel:[1,0,0]
	v_mov_b32_e32 v238, v195
	v_pk_fma_f32 v[0:1], v[194:195], v[44:45], v[0:1] op_sel_hi:[0,1,1]
	v_pk_fma_f32 v[0:1], v[238:239], v[46:47], v[0:1] op_sel_hi:[0,1,1]
	s_waitcnt lgkmcnt(2)
	v_pk_fma_f32 v[0:1], v[196:197], v[48:49], v[0:1] op_sel_hi:[0,1,1]
	v_pk_fma_f32 v[0:1], v[196:197], v[50:51], v[0:1] op_sel:[1,0,0]
	v_mov_b32_e32 v240, v199
	v_pk_fma_f32 v[0:1], v[198:199], v[52:53], v[0:1] op_sel_hi:[0,1,1]
	v_pk_fma_f32 v[0:1], v[240:241], v[54:55], v[0:1] op_sel_hi:[0,1,1]
	s_waitcnt lgkmcnt(1)
	v_pk_fma_f32 v[0:1], v[222:223], v[56:57], v[0:1] op_sel_hi:[0,1,1]
	v_pk_fma_f32 v[0:1], v[222:223], v[58:59], v[0:1] op_sel:[1,0,0]
	v_mov_b32_e32 v242, v225
	v_pk_fma_f32 v[0:1], v[224:225], v[60:61], v[0:1] op_sel_hi:[0,1,1]
	v_pk_fma_f32 v[0:1], v[242:243], v[62:63], v[0:1] op_sel_hi:[0,1,1]
	s_waitcnt lgkmcnt(0)
	v_pk_fma_f32 v[0:1], v[226:227], v[64:65], v[0:1] op_sel_hi:[0,1,1]
	v_pk_fma_f32 v[0:1], v[226:227], v[66:67], v[0:1] op_sel:[1,0,0]
	v_mov_b32_e32 v2, v229
	v_pk_fma_f32 v[0:1], v[228:229], v[68:69], v[0:1] op_sel_hi:[0,1,1]
	v_pk_fma_f32 v[190:191], v[2:3], v[70:71], v[0:1] op_sel_hi:[0,1,1]
	ds_read_b128 v[0:3], v210 offset:144
	ds_read_b128 v[4:7], v210 offset:160
	ds_read_b128 v[182:185], v210 offset:176
	ds_read_b128 v[186:189], v210 offset:192
	s_waitcnt lgkmcnt(3)
	v_pk_fma_f32 v[190:191], v[0:1], v[72:73], v[190:191] op_sel_hi:[0,1,1]
	v_pk_fma_f32 v[0:1], v[0:1], v[74:75], v[190:191] op_sel:[1,0,0]
	v_mov_b32_e32 v192, v3
	v_pk_fma_f32 v[0:1], v[2:3], v[76:77], v[0:1] op_sel_hi:[0,1,1]
	v_pk_fma_f32 v[0:1], v[192:193], v[78:79], v[0:1] op_sel_hi:[0,1,1]
	s_waitcnt lgkmcnt(2)
	v_pk_fma_f32 v[0:1], v[4:5], v[80:81], v[0:1] op_sel_hi:[0,1,1]
	v_pk_fma_f32 v[0:1], v[4:5], v[82:83], v[0:1] op_sel:[1,0,0]
	v_mov_b32_e32 v2, v7
	v_pk_fma_f32 v[0:1], v[6:7], v[84:85], v[0:1] op_sel_hi:[0,1,1]
	v_pk_fma_f32 v[0:1], v[2:3], v[86:87], v[0:1] op_sel_hi:[0,1,1]
	s_waitcnt lgkmcnt(1)
	v_pk_fma_f32 v[0:1], v[182:183], v[88:89], v[0:1] op_sel_hi:[0,1,1]
	v_pk_fma_f32 v[0:1], v[182:183], v[90:91], v[0:1] op_sel:[1,0,0]
	v_mov_b32_e32 v2, v185
	v_pk_fma_f32 v[0:1], v[184:185], v[92:93], v[0:1] op_sel_hi:[0,1,1]
	v_pk_fma_f32 v[0:1], v[2:3], v[94:95], v[0:1] op_sel_hi:[0,1,1]
	s_waitcnt lgkmcnt(0)
	v_pk_fma_f32 v[0:1], v[186:187], v[96:97], v[0:1] op_sel_hi:[0,1,1]
	v_pk_fma_f32 v[4:5], v[186:187], v[98:99], v[0:1] op_sel:[1,0,0]
	ds_read_b128 v[0:3], v210 offset:208
	v_pk_fma_f32 v[4:5], v[188:189], v[100:101], v[4:5] op_sel_hi:[0,1,1]
	v_mov_b32_e32 v6, v189
	v_pk_fma_f32 v[182:183], v[6:7], v[102:103], v[4:5] op_sel_hi:[0,1,1]
	ds_read_b128 v[4:7], v210 offset:224
	s_waitcnt lgkmcnt(1)
	v_pk_fma_f32 v[182:183], v[0:1], v[104:105], v[182:183] op_sel_hi:[0,1,1]
	v_pk_fma_f32 v[0:1], v[0:1], v[106:107], v[182:183] op_sel:[1,0,0]
	s_nop 0
	v_pk_fma_f32 v[0:1], v[2:3], v[108:109], v[0:1] op_sel_hi:[0,1,1]
	v_mov_b32_e32 v2, v3
	v_pk_fma_f32 v[0:1], v[2:3], v[110:111], v[0:1] op_sel_hi:[0,1,1]
	s_waitcnt lgkmcnt(0)
	v_pk_fma_f32 v[0:1], v[4:5], v[112:113], v[0:1] op_sel_hi:[0,1,1]
	v_pk_fma_f32 v[4:5], v[4:5], v[114:115], v[0:1] op_sel:[1,0,0]
	ds_read_b128 v[0:3], v210 offset:240
	v_pk_fma_f32 v[4:5], v[6:7], v[116:117], v[4:5] op_sel_hi:[0,1,1]
	v_mov_b32_e32 v6, v7
	v_pk_fma_f32 v[182:183], v[6:7], v[118:119], v[4:5] op_sel_hi:[0,1,1]
	ds_read_b128 v[4:7], v210 offset:256
	s_waitcnt lgkmcnt(1)
	v_pk_fma_f32 v[182:183], v[0:1], v[120:121], v[182:183] op_sel_hi:[0,1,1]
	v_pk_fma_f32 v[0:1], v[0:1], v[122:123], v[182:183] op_sel:[1,0,0]
	s_nop 0
	v_pk_fma_f32 v[0:1], v[2:3], v[124:125], v[0:1] op_sel_hi:[0,1,1]
	v_mov_b32_e32 v2, v3
	v_pk_fma_f32 v[0:1], v[2:3], v[126:127], v[0:1] op_sel_hi:[0,1,1]
	s_waitcnt lgkmcnt(0)
	v_pk_fma_f32 v[0:1], v[4:5], v[128:129], v[0:1] op_sel_hi:[0,1,1]
	v_pk_fma_f32 v[0:1], v[4:5], v[130:131], v[0:1] op_sel:[1,0,0]
	v_mov_b32_e32 v2, v7
	v_pk_fma_f32 v[0:1], v[6:7], v[132:133], v[0:1] op_sel_hi:[0,1,1]
	v_pk_fma_f32 v[0:1], v[2:3], v[134:135], v[0:1] op_sel_hi:[0,1,1]
	ds_read_b128 v[2:5], v210 offset:8208
	ds_read_b128 v[182:185], v210 offset:8224
	ds_read_b128 v[186:189], v210 offset:8240
	ds_read_b128 v[192:195], v210 offset:8256
	s_waitcnt lgkmcnt(3)
	v_pk_fma_f32 v[6:7], v[2:3], v[8:9], 0 op_sel_hi:[0,1,0]
	v_pk_fma_f32 v[2:3], v[2:3], v[10:11], v[6:7] op_sel:[1,0,0]
	v_mov_b32_e32 v190, v5
	v_pk_fma_f32 v[2:3], v[4:5], v[12:13], v[2:3] op_sel_hi:[0,1,1]
	v_pk_fma_f32 v[2:3], v[190:191], v[14:15], v[2:3] op_sel_hi:[0,1,1]
	s_waitcnt lgkmcnt(2)
	v_pk_fma_f32 v[2:3], v[182:183], v[16:17], v[2:3] op_sel_hi:[0,1,1]
	v_pk_fma_f32 v[2:3], v[182:183], v[18:19], v[2:3] op_sel:[1,0,0]
	v_mov_b32_e32 v4, v185
	v_pk_fma_f32 v[2:3], v[184:185], v[20:21], v[2:3] op_sel_hi:[0,1,1]
	v_pk_fma_f32 v[2:3], v[4:5], v[22:23], v[2:3] op_sel_hi:[0,1,1]
	s_waitcnt lgkmcnt(1)
	v_pk_fma_f32 v[2:3], v[186:187], v[24:25], v[2:3] op_sel_hi:[0,1,1]
	v_pk_fma_f32 v[2:3], v[186:187], v[26:27], v[2:3] op_sel:[1,0,0]
	v_mov_b32_e32 v4, v189
	v_pk_fma_f32 v[2:3], v[188:189], v[28:29], v[2:3] op_sel_hi:[0,1,1]
	v_pk_fma_f32 v[2:3], v[4:5], v[30:31], v[2:3] op_sel_hi:[0,1,1]
	s_waitcnt lgkmcnt(0)
	v_pk_fma_f32 v[2:3], v[192:193], v[32:33], v[2:3] op_sel_hi:[0,1,1]
	v_pk_fma_f32 v[6:7], v[192:193], v[34:35], v[2:3] op_sel:[1,0,0]
	ds_read_b128 v[2:5], v210 offset:8272
	v_pk_fma_f32 v[6:7], v[194:195], v[36:37], v[6:7] op_sel_hi:[0,1,1]
	v_mov_b32_e32 v182, v195
	v_pk_fma_f32 v[6:7], v[182:183], v[38:39], v[6:7] op_sel_hi:[0,1,1]
	ds_read_b128 v[182:185], v210 offset:8288
	s_waitcnt lgkmcnt(1)
; template <bool DRY = false>
; DI void phase_ln_router(const Params& p, char* smem, int bid, int nb) {
;     ...
;       f32x2_t acc[8];
; #pragma unroll
;       for (int j = 0; j < 8; ++j) acc[j] = (f32x2_t){0.f, 0.f};
; #pragma unroll
;       for (int j = 0; j < 8; ++j) {
; #pragma unroll
;         for (int i4 = 0; i4 < 16; ++i4) {
;           const float4 h = *(const float4*)(hs + j * 2048 + ks * 64 + 4 * i4);
;           acc[j] = __builtin_elementwise_fma((f32x2_t){h.x, h.x}, wr[4 * i4], acc[j]); acc[j] = __builtin_elementwise_fma((f32x2_t){h.y, h.y}, wr[4 * i4 + 1], acc[j]);
;           acc[j] = __builtin_elementwise_fma((f32x2_t){h.z, h.z}, wr[4 * i4 + 2], acc[j]); acc[j] = __builtin_elementwise_fma((f32x2_t){h.w, h.w}, wr[4 * i4 + 3], acc[j]);
;           if ((i4 & 7) == 7) __builtin_amdgcn_sched_barrier(0);
;         }
;       }
	v_pk_fma_f32 v[6:7], v[2:3], v[40:41], v[6:7] op_sel_hi:[0,1,1]
	v_pk_fma_f32 v[2:3], v[2:3], v[42:43], v[6:7] op_sel:[1,0,0]
	s_nop 0
	v_pk_fma_f32 v[2:3], v[4:5], v[44:45], v[2:3] op_sel_hi:[0,1,1]
	v_mov_b32_e32 v4, v5
	v_pk_fma_f32 v[2:3], v[4:5], v[46:47], v[2:3] op_sel_hi:[0,1,1]
	s_waitcnt lgkmcnt(0)
	v_pk_fma_f32 v[2:3], v[182:183], v[48:49], v[2:3] op_sel_hi:[0,1,1]
	v_pk_fma_f32 v[6:7], v[182:183], v[50:51], v[2:3] op_sel:[1,0,0]
	ds_read_b128 v[2:5], v210 offset:8304
	v_pk_fma_f32 v[6:7], v[184:185], v[52:53], v[6:7] op_sel_hi:[0,1,1]
	v_mov_b32_e32 v182, v185
	v_pk_fma_f32 v[6:7], v[182:183], v[54:55], v[6:7] op_sel_hi:[0,1,1]
	ds_read_b128 v[182:185], v210 offset:8320
	s_waitcnt lgkmcnt(1)
	v_pk_fma_f32 v[6:7], v[2:3], v[56:57], v[6:7] op_sel_hi:[0,1,1]
	v_pk_fma_f32 v[2:3], v[2:3], v[58:59], v[6:7] op_sel:[1,0,0]
	s_nop 0
	v_pk_fma_f32 v[2:3], v[4:5], v[60:61], v[2:3] op_sel_hi:[0,1,1]
	v_mov_b32_e32 v4, v5
	v_pk_fma_f32 v[2:3], v[4:5], v[62:63], v[2:3] op_sel_hi:[0,1,1]
	s_waitcnt lgkmcnt(0)
	v_pk_fma_f32 v[2:3], v[182:183], v[64:65], v[2:3] op_sel_hi:[0,1,1]
	v_pk_fma_f32 v[2:3], v[182:183], v[66:67], v[2:3] op_sel:[1,0,0]
	v_mov_b32_e32 v4, v185
	v_pk_fma_f32 v[2:3], v[184:185], v[68:69], v[2:3] op_sel_hi:[0,1,1]
	v_pk_fma_f32 v[6:7], v[4:5], v[70:71], v[2:3] op_sel_hi:[0,1,1]
	ds_read_b128 v[2:5], v210 offset:8336
	ds_read_b128 v[182:185], v210 offset:8352
	ds_read_b128 v[186:189], v210 offset:8368
	ds_read_b128 v[192:195], v210 offset:8384
	s_waitcnt lgkmcnt(3)
	v_pk_fma_f32 v[6:7], v[2:3], v[72:73], v[6:7] op_sel_hi:[0,1,1]
	v_pk_fma_f32 v[2:3], v[2:3], v[74:75], v[6:7] op_sel:[1,0,0]
	v_mov_b32_e32 v190, v5
	v_pk_fma_f32 v[2:3], v[4:5], v[76:77], v[2:3] op_sel_hi:[0,1,1]
	v_pk_fma_f32 v[2:3], v[190:191], v[78:79], v[2:3] op_sel_hi:[0,1,1]
	s_waitcnt lgkmcnt(2)
	v_pk_fma_f32 v[2:3], v[182:183], v[80:81], v[2:3] op_sel_hi:[0,1,1]
	v_pk_fma_f32 v[2:3], v[182:183], v[82:83], v[2:3] op_sel:[1,0,0]
	v_mov_b32_e32 v4, v185
	v_pk_fma_f32 v[2:3], v[184:185], v[84:85], v[2:3] op_sel_hi:[0,1,1]
	v_pk_fma_f32 v[2:3], v[4:5], v[86:87], v[2:3] op_sel_hi:[0,1,1]
	s_waitcnt lgkmcnt(1)
	v_pk_fma_f32 v[2:3], v[186:187], v[88:89], v[2:3] op_sel_hi:[0,1,1]
	v_pk_fma_f32 v[2:3], v[186:187], v[90:91], v[2:3] op_sel:[1,0,0]
	v_mov_b32_e32 v4, v189
	v_pk_fma_f32 v[2:3], v[188:189], v[92:93], v[2:3] op_sel_hi:[0,1,1]
	v_pk_fma_f32 v[2:3], v[4:5], v[94:95], v[2:3] op_sel_hi:[0,1,1]
	s_waitcnt lgkmcnt(0)
	v_pk_fma_f32 v[2:3], v[192:193], v[96:97], v[2:3] op_sel_hi:[0,1,1]
	v_pk_fma_f32 v[6:7], v[192:193], v[98:99], v[2:3] op_sel:[1,0,0]
	ds_read_b128 v[2:5], v210 offset:8400
	v_pk_fma_f32 v[6:7], v[194:195], v[100:101], v[6:7] op_sel_hi:[0,1,1]
	v_mov_b32_e32 v182, v195
	v_pk_fma_f32 v[6:7], v[182:183], v[102:103], v[6:7] op_sel_hi:[0,1,1]
	ds_read_b128 v[182:185], v210 offset:8416
	s_waitcnt lgkmcnt(1)
	v_pk_fma_f32 v[6:7], v[2:3], v[104:105], v[6:7] op_sel_hi:[0,1,1]
	v_pk_fma_f32 v[2:3], v[2:3], v[106:107], v[6:7] op_sel:[1,0,0]
	s_nop 0
	v_pk_fma_f32 v[2:3], v[4:5], v[108:109], v[2:3] op_sel_hi:[0,1,1]
	v_mov_b32_e32 v4, v5
	v_pk_fma_f32 v[2:3], v[4:5], v[110:111], v[2:3] op_sel_hi:[0,1,1]
	s_waitcnt lgkmcnt(0)
	v_pk_fma_f32 v[2:3], v[182:183], v[112:113], v[2:3] op_sel_hi:[0,1,1]
	v_pk_fma_f32 v[6:7], v[182:183], v[114:115], v[2:3] op_sel:[1,0,0]
	ds_read_b128 v[2:5], v210 offset:8432
	v_pk_fma_f32 v[6:7], v[184:185], v[116:117], v[6:7] op_sel_hi:[0,1,1]
	v_mov_b32_e32 v182, v185
	v_pk_fma_f32 v[6:7], v[182:183], v[118:119], v[6:7] op_sel_hi:[0,1,1]
	ds_read_b128 v[182:185], v210 offset:8448
	s_waitcnt lgkmcnt(1)
	v_pk_fma_f32 v[6:7], v[2:3], v[120:121], v[6:7] op_sel_hi:[0,1,1]
	v_pk_fma_f32 v[2:3], v[2:3], v[122:123], v[6:7] op_sel:[1,0,0]
	s_nop 0
	v_pk_fma_f32 v[2:3], v[4:5], v[124:125], v[2:3] op_sel_hi:[0,1,1]
	v_mov_b32_e32 v4, v5
	v_pk_fma_f32 v[2:3], v[4:5], v[126:127], v[2:3] op_sel_hi:[0,1,1]
	s_waitcnt lgkmcnt(0)
	v_pk_fma_f32 v[2:3], v[182:183], v[128:129], v[2:3] op_sel_hi:[0,1,1]
	v_pk_fma_f32 v[2:3], v[182:183], v[130:131], v[2:3] op_sel:[1,0,0]
	v_mov_b32_e32 v4, v185
	v_pk_fma_f32 v[2:3], v[184:185], v[132:133], v[2:3] op_sel_hi:[0,1,1]
	v_pk_fma_f32 v[2:3], v[4:5], v[134:135], v[2:3] op_sel_hi:[0,1,1]
	ds_read_b128 v[4:7], v210 offset:16400
	ds_read_b128 v[182:185], v210 offset:16416
	ds_read_b128 v[186:189], v210 offset:16432
	ds_read_b128 v[192:195], v210 offset:16448
	s_waitcnt lgkmcnt(3)
	v_pk_fma_f32 v[190:191], v[4:5], v[8:9], 0 op_sel_hi:[0,1,0]
	v_pk_fma_f32 v[4:5], v[4:5], v[10:11], v[190:191] op_sel:[1,0,0]
	v_mov_b32_e32 v196, v7
	v_pk_fma_f32 v[4:5], v[6:7], v[12:13], v[4:5] op_sel_hi:[0,1,1]
	v_pk_fma_f32 v[4:5], v[196:197], v[14:15], v[4:5] op_sel_hi:[0,1,1]
	s_waitcnt lgkmcnt(2)
	v_pk_fma_f32 v[4:5], v[182:183], v[16:17], v[4:5] op_sel_hi:[0,1,1]
	v_pk_fma_f32 v[4:5], v[182:183], v[18:19], v[4:5] op_sel:[1,0,0]
	v_mov_b32_e32 v6, v185
	v_pk_fma_f32 v[4:5], v[184:185], v[20:21], v[4:5] op_sel_hi:[0,1,1]
	v_pk_fma_f32 v[4:5], v[6:7], v[22:23], v[4:5] op_sel_hi:[0,1,1]
	s_waitcnt lgkmcnt(1)
	v_pk_fma_f32 v[4:5], v[186:187], v[24:25], v[4:5] op_sel_hi:[0,1,1]
	v_pk_fma_f32 v[4:5], v[186:187], v[26:27], v[4:5] op_sel:[1,0,0]
	v_mov_b32_e32 v6, v189
	v_pk_fma_f32 v[4:5], v[188:189], v[28:29], v[4:5] op_sel_hi:[0,1,1]
	v_pk_fma_f32 v[4:5], v[6:7], v[30:31], v[4:5] op_sel_hi:[0,1,1]
	s_waitcnt lgkmcnt(0)
	v_pk_fma_f32 v[4:5], v[192:193], v[32:33], v[4:5] op_sel_hi:[0,1,1]
	v_pk_fma_f32 v[182:183], v[192:193], v[34:35], v[4:5] op_sel:[1,0,0]
	ds_read_b128 v[4:7], v210 offset:16464
	v_pk_fma_f32 v[182:183], v[194:195], v[36:37], v[182:183] op_sel_hi:[0,1,1]
	v_mov_b32_e32 v184, v195
	v_pk_fma_f32 v[186:187], v[184:185], v[38:39], v[182:183] op_sel_hi:[0,1,1]
	ds_read_b128 v[182:185], v210 offset:16480
	s_waitcnt lgkmcnt(1)
; template <bool DRY = false>
; DI void phase_ln_router(const Params& p, char* smem, int bid, int nb) {
;     ...
;       f32x2_t acc[8];
; #pragma unroll
;       for (int j = 0; j < 8; ++j) acc[j] = (f32x2_t){0.f, 0.f};
; #pragma unroll
;       for (int j = 0; j < 8; ++j) {
; #pragma unroll
;         for (int i4 = 0; i4 < 16; ++i4) {
;           const float4 h = *(const float4*)(hs + j * 2048 + ks * 64 + 4 * i4);
;           acc[j] = __builtin_elementwise_fma((f32x2_t){h.x, h.x}, wr[4 * i4], acc[j]); acc[j] = __builtin_elementwise_fma((f32x2_t){h.y, h.y}, wr[4 * i4 + 1], acc[j]);
;           acc[j] = __builtin_elementwise_fma((f32x2_t){h.z, h.z}, wr[4 * i4 + 2], acc[j]); acc[j] = __builtin_elementwise_fma((f32x2_t){h.w, h.w}, wr[4 * i4 + 3], acc[j]);
;           if ((i4 & 7) == 7) __builtin_amdgcn_sched_barrier(0);
;         }
;       }
	v_pk_fma_f32 v[186:187], v[4:5], v[40:41], v[186:187] op_sel_hi:[0,1,1]
	v_pk_fma_f32 v[4:5], v[4:5], v[42:43], v[186:187] op_sel:[1,0,0]
	s_nop 0
	v_pk_fma_f32 v[4:5], v[6:7], v[44:45], v[4:5] op_sel_hi:[0,1,1]
	v_mov_b32_e32 v6, v7
	v_pk_fma_f32 v[4:5], v[6:7], v[46:47], v[4:5] op_sel_hi:[0,1,1]
	s_waitcnt lgkmcnt(0)
	v_pk_fma_f32 v[4:5], v[182:183], v[48:49], v[4:5] op_sel_hi:[0,1,1]
	v_pk_fma_f32 v[182:183], v[182:183], v[50:51], v[4:5] op_sel:[1,0,0]
	ds_read_b128 v[4:7], v210 offset:16496
	v_pk_fma_f32 v[182:183], v[184:185], v[52:53], v[182:183] op_sel_hi:[0,1,1]
	v_mov_b32_e32 v184, v185
	v_pk_fma_f32 v[186:187], v[184:185], v[54:55], v[182:183] op_sel_hi:[0,1,1]
	ds_read_b128 v[182:185], v210 offset:16512
	s_waitcnt lgkmcnt(1)
	v_pk_fma_f32 v[186:187], v[4:5], v[56:57], v[186:187] op_sel_hi:[0,1,1]
	v_pk_fma_f32 v[4:5], v[4:5], v[58:59], v[186:187] op_sel:[1,0,0]
	s_nop 0
	v_pk_fma_f32 v[4:5], v[6:7], v[60:61], v[4:5] op_sel_hi:[0,1,1]
	v_mov_b32_e32 v6, v7
	v_pk_fma_f32 v[4:5], v[6:7], v[62:63], v[4:5] op_sel_hi:[0,1,1]
	s_waitcnt lgkmcnt(0)
	v_pk_fma_f32 v[4:5], v[182:183], v[64:65], v[4:5] op_sel_hi:[0,1,1]
	v_pk_fma_f32 v[4:5], v[182:183], v[66:67], v[4:5] op_sel:[1,0,0]
	v_mov_b32_e32 v6, v185
	v_pk_fma_f32 v[4:5], v[184:185], v[68:69], v[4:5] op_sel_hi:[0,1,1]
	v_pk_fma_f32 v[190:191], v[6:7], v[70:71], v[4:5] op_sel_hi:[0,1,1]
	ds_read_b128 v[4:7], v210 offset:16528
	ds_read_b128 v[182:185], v210 offset:16544
	ds_read_b128 v[186:189], v210 offset:16560
	ds_read_b128 v[192:195], v210 offset:16576
	s_waitcnt lgkmcnt(3)
	v_pk_fma_f32 v[190:191], v[4:5], v[72:73], v[190:191] op_sel_hi:[0,1,1]
	v_pk_fma_f32 v[4:5], v[4:5], v[74:75], v[190:191] op_sel:[1,0,0]
	v_mov_b32_e32 v196, v7
	v_pk_fma_f32 v[4:5], v[6:7], v[76:77], v[4:5] op_sel_hi:[0,1,1]
	v_pk_fma_f32 v[4:5], v[196:197], v[78:79], v[4:5] op_sel_hi:[0,1,1]
	s_waitcnt lgkmcnt(2)
	v_pk_fma_f32 v[4:5], v[182:183], v[80:81], v[4:5] op_sel_hi:[0,1,1]
	v_pk_fma_f32 v[4:5], v[182:183], v[82:83], v[4:5] op_sel:[1,0,0]
	v_mov_b32_e32 v6, v185
	v_pk_fma_f32 v[4:5], v[184:185], v[84:85], v[4:5] op_sel_hi:[0,1,1]
	v_pk_fma_f32 v[4:5], v[6:7], v[86:87], v[4:5] op_sel_hi:[0,1,1]
	s_waitcnt lgkmcnt(1)
	v_pk_fma_f32 v[4:5], v[186:187], v[88:89], v[4:5] op_sel_hi:[0,1,1]
	v_pk_fma_f32 v[4:5], v[186:187], v[90:91], v[4:5] op_sel:[1,0,0]
	v_mov_b32_e32 v6, v189
	v_pk_fma_f32 v[4:5], v[188:189], v[92:93], v[4:5] op_sel_hi:[0,1,1]
	v_pk_fma_f32 v[4:5], v[6:7], v[94:95], v[4:5] op_sel_hi:[0,1,1]
	s_waitcnt lgkmcnt(0)
	v_pk_fma_f32 v[4:5], v[192:193], v[96:97], v[4:5] op_sel_hi:[0,1,1]
	v_pk_fma_f32 v[182:183], v[192:193], v[98:99], v[4:5] op_sel:[1,0,0]
	ds_read_b128 v[4:7], v210 offset:16592
	v_pk_fma_f32 v[182:183], v[194:195], v[100:101], v[182:183] op_sel_hi:[0,1,1]
	v_mov_b32_e32 v184, v195
	v_pk_fma_f32 v[186:187], v[184:185], v[102:103], v[182:183] op_sel_hi:[0,1,1]
	ds_read_b128 v[182:185], v210 offset:16608
	s_waitcnt lgkmcnt(1)
	v_pk_fma_f32 v[186:187], v[4:5], v[104:105], v[186:187] op_sel_hi:[0,1,1]
	v_pk_fma_f32 v[4:5], v[4:5], v[106:107], v[186:187] op_sel:[1,0,0]
	s_nop 0
	v_pk_fma_f32 v[4:5], v[6:7], v[108:109], v[4:5] op_sel_hi:[0,1,1]
	v_mov_b32_e32 v6, v7
	v_pk_fma_f32 v[4:5], v[6:7], v[110:111], v[4:5] op_sel_hi:[0,1,1]
	s_waitcnt lgkmcnt(0)
	v_pk_fma_f32 v[4:5], v[182:183], v[112:113], v[4:5] op_sel_hi:[0,1,1]
	v_pk_fma_f32 v[182:183], v[182:183], v[114:115], v[4:5] op_sel:[1,0,0]
	ds_read_b128 v[4:7], v210 offset:16624
	v_pk_fma_f32 v[182:183], v[184:185], v[116:117], v[182:183] op_sel_hi:[0,1,1]
	v_mov_b32_e32 v184, v185
	v_pk_fma_f32 v[186:187], v[184:185], v[118:119], v[182:183] op_sel_hi:[0,1,1]
	ds_read_b128 v[182:185], v210 offset:16640
	s_waitcnt lgkmcnt(1)
	v_pk_fma_f32 v[186:187], v[4:5], v[120:121], v[186:187] op_sel_hi:[0,1,1]
	v_pk_fma_f32 v[4:5], v[4:5], v[122:123], v[186:187] op_sel:[1,0,0]
	s_nop 0
	v_pk_fma_f32 v[4:5], v[6:7], v[124:125], v[4:5] op_sel_hi:[0,1,1]
	v_mov_b32_e32 v6, v7
	v_pk_fma_f32 v[4:5], v[6:7], v[126:127], v[4:5] op_sel_hi:[0,1,1]
	s_waitcnt lgkmcnt(0)
	v_pk_fma_f32 v[4:5], v[182:183], v[128:129], v[4:5] op_sel_hi:[0,1,1]
	v_pk_fma_f32 v[4:5], v[182:183], v[130:131], v[4:5] op_sel:[1,0,0]
	v_mov_b32_e32 v6, v185
	v_pk_fma_f32 v[4:5], v[184:185], v[132:133], v[4:5] op_sel_hi:[0,1,1]
	v_pk_fma_f32 v[4:5], v[6:7], v[134:135], v[4:5] op_sel_hi:[0,1,1]
	ds_read_b128 v[182:185], v210 offset:24592
	ds_read_b128 v[186:189], v210 offset:24608
	ds_read_b128 v[192:195], v210 offset:24624
	ds_read_b128 v[196:199], v210 offset:24640
	s_waitcnt lgkmcnt(3)
	v_pk_fma_f32 v[6:7], v[182:183], v[8:9], 0 op_sel_hi:[0,1,0]
	v_pk_fma_f32 v[6:7], v[182:183], v[10:11], v[6:7] op_sel:[1,0,0]
	v_mov_b32_e32 v190, v185
	v_pk_fma_f32 v[6:7], v[184:185], v[12:13], v[6:7] op_sel_hi:[0,1,1]
	v_pk_fma_f32 v[6:7], v[190:191], v[14:15], v[6:7] op_sel_hi:[0,1,1]
	s_waitcnt lgkmcnt(2)
	v_pk_fma_f32 v[6:7], v[186:187], v[16:17], v[6:7] op_sel_hi:[0,1,1]
	v_pk_fma_f32 v[6:7], v[186:187], v[18:19], v[6:7] op_sel:[1,0,0]
	v_mov_b32_e32 v182, v189
	v_pk_fma_f32 v[6:7], v[188:189], v[20:21], v[6:7] op_sel_hi:[0,1,1]
	v_pk_fma_f32 v[6:7], v[182:183], v[22:23], v[6:7] op_sel_hi:[0,1,1]
	s_waitcnt lgkmcnt(1)
	v_pk_fma_f32 v[6:7], v[192:193], v[24:25], v[6:7] op_sel_hi:[0,1,1]
	v_pk_fma_f32 v[6:7], v[192:193], v[26:27], v[6:7] op_sel:[1,0,0]
	v_mov_b32_e32 v182, v195
	v_pk_fma_f32 v[6:7], v[194:195], v[28:29], v[6:7] op_sel_hi:[0,1,1]
	v_pk_fma_f32 v[6:7], v[182:183], v[30:31], v[6:7] op_sel_hi:[0,1,1]
	ds_read_b128 v[182:185], v210 offset:24656
	s_waitcnt lgkmcnt(1)
; template <bool DRY = false>
; DI void phase_ln_router(const Params& p, char* smem, int bid, int nb) {
;     ...
;       f32x2_t acc[8];
; #pragma unroll
;       for (int j = 0; j < 8; ++j) acc[j] = (f32x2_t){0.f, 0.f};
; #pragma unroll
;       for (int j = 0; j < 8; ++j) {
; #pragma unroll
;         for (int i4 = 0; i4 < 16; ++i4) {
;           const float4 h = *(const float4*)(hs + j * 2048 + ks * 64 + 4 * i4);
;           acc[j] = __builtin_elementwise_fma((f32x2_t){h.x, h.x}, wr[4 * i4], acc[j]); acc[j] = __builtin_elementwise_fma((f32x2_t){h.y, h.y}, wr[4 * i4 + 1], acc[j]);
;           acc[j] = __builtin_elementwise_fma((f32x2_t){h.z, h.z}, wr[4 * i4 + 2], acc[j]); acc[j] = __builtin_elementwise_fma((f32x2_t){h.w, h.w}, wr[4 * i4 + 3], acc[j]);
;           if ((i4 & 7) == 7) __builtin_amdgcn_sched_barrier(0);
;         }
;       }
	v_pk_fma_f32 v[6:7], v[196:197], v[32:33], v[6:7] op_sel_hi:[0,1,1]
	v_pk_fma_f32 v[6:7], v[196:197], v[34:35], v[6:7] op_sel:[1,0,0]
	v_mov_b32_e32 v186, v199
	v_pk_fma_f32 v[6:7], v[198:199], v[36:37], v[6:7] op_sel_hi:[0,1,1]
	v_pk_fma_f32 v[6:7], v[186:187], v[38:39], v[6:7] op_sel_hi:[0,1,1]
	ds_read_b128 v[186:189], v210 offset:24672
	s_waitcnt lgkmcnt(1)
	v_pk_fma_f32 v[6:7], v[182:183], v[40:41], v[6:7] op_sel_hi:[0,1,1]
	v_pk_fma_f32 v[6:7], v[182:183], v[42:43], v[6:7] op_sel:[1,0,0]
	v_mov_b32_e32 v182, v185
	v_pk_fma_f32 v[6:7], v[184:185], v[44:45], v[6:7] op_sel_hi:[0,1,1]
	v_pk_fma_f32 v[6:7], v[182:183], v[46:47], v[6:7] op_sel_hi:[0,1,1]
	ds_read_b128 v[182:185], v210 offset:24688
	s_waitcnt lgkmcnt(1)
	v_pk_fma_f32 v[6:7], v[186:187], v[48:49], v[6:7] op_sel_hi:[0,1,1]
	v_pk_fma_f32 v[6:7], v[186:187], v[50:51], v[6:7] op_sel:[1,0,0]
	v_mov_b32_e32 v186, v189
	v_pk_fma_f32 v[6:7], v[188:189], v[52:53], v[6:7] op_sel_hi:[0,1,1]
	v_pk_fma_f32 v[6:7], v[186:187], v[54:55], v[6:7] op_sel_hi:[0,1,1]
	ds_read_b128 v[186:189], v210 offset:24704
	s_waitcnt lgkmcnt(1)
	v_pk_fma_f32 v[6:7], v[182:183], v[56:57], v[6:7] op_sel_hi:[0,1,1]
	v_pk_fma_f32 v[6:7], v[182:183], v[58:59], v[6:7] op_sel:[1,0,0]
	v_mov_b32_e32 v182, v185
	v_pk_fma_f32 v[6:7], v[184:185], v[60:61], v[6:7] op_sel_hi:[0,1,1]
	v_pk_fma_f32 v[6:7], v[182:183], v[62:63], v[6:7] op_sel_hi:[0,1,1]
	s_waitcnt lgkmcnt(0)
	v_pk_fma_f32 v[6:7], v[186:187], v[64:65], v[6:7] op_sel_hi:[0,1,1]
	v_pk_fma_f32 v[6:7], v[186:187], v[66:67], v[6:7] op_sel:[1,0,0]
	v_mov_b32_e32 v182, v189
	v_pk_fma_f32 v[6:7], v[188:189], v[68:69], v[6:7] op_sel_hi:[0,1,1]
	v_pk_fma_f32 v[6:7], v[182:183], v[70:71], v[6:7] op_sel_hi:[0,1,1]
	ds_read_b128 v[182:185], v210 offset:24720
	ds_read_b128 v[186:189], v210 offset:24736
	ds_read_b128 v[192:195], v210 offset:24752
	ds_read_b128 v[196:199], v210 offset:24768
	s_waitcnt lgkmcnt(3)
	v_pk_fma_f32 v[6:7], v[182:183], v[72:73], v[6:7] op_sel_hi:[0,1,1]
	v_pk_fma_f32 v[6:7], v[182:183], v[74:75], v[6:7] op_sel:[1,0,0]
	v_mov_b32_e32 v190, v185
	v_pk_fma_f32 v[6:7], v[184:185], v[76:77], v[6:7] op_sel_hi:[0,1,1]
	v_pk_fma_f32 v[6:7], v[190:191], v[78:79], v[6:7] op_sel_hi:[0,1,1]
	s_waitcnt lgkmcnt(2)
	v_pk_fma_f32 v[6:7], v[186:187], v[80:81], v[6:7] op_sel_hi:[0,1,1]
	v_pk_fma_f32 v[6:7], v[186:187], v[82:83], v[6:7] op_sel:[1,0,0]
	v_mov_b32_e32 v182, v189
	v_pk_fma_f32 v[6:7], v[188:189], v[84:85], v[6:7] op_sel_hi:[0,1,1]
	v_pk_fma_f32 v[6:7], v[182:183], v[86:87], v[6:7] op_sel_hi:[0,1,1]
	s_waitcnt lgkmcnt(1)
	v_pk_fma_f32 v[6:7], v[192:193], v[88:89], v[6:7] op_sel_hi:[0,1,1]
	v_pk_fma_f32 v[6:7], v[192:193], v[90:91], v[6:7] op_sel:[1,0,0]
	v_mov_b32_e32 v182, v195
	v_pk_fma_f32 v[6:7], v[194:195], v[92:93], v[6:7] op_sel_hi:[0,1,1]
	v_pk_fma_f32 v[6:7], v[182:183], v[94:95], v[6:7] op_sel_hi:[0,1,1]
	ds_read_b128 v[182:185], v210 offset:24784
	s_waitcnt lgkmcnt(1)
	v_pk_fma_f32 v[6:7], v[196:197], v[96:97], v[6:7] op_sel_hi:[0,1,1]
	v_pk_fma_f32 v[6:7], v[196:197], v[98:99], v[6:7] op_sel:[1,0,0]
	v_mov_b32_e32 v186, v199
	v_pk_fma_f32 v[6:7], v[198:199], v[100:101], v[6:7] op_sel_hi:[0,1,1]
	v_pk_fma_f32 v[6:7], v[186:187], v[102:103], v[6:7] op_sel_hi:[0,1,1]
	ds_read_b128 v[186:189], v210 offset:24800
	s_waitcnt lgkmcnt(1)
	v_pk_fma_f32 v[6:7], v[182:183], v[104:105], v[6:7] op_sel_hi:[0,1,1]
	v_pk_fma_f32 v[6:7], v[182:183], v[106:107], v[6:7] op_sel:[1,0,0]
	v_mov_b32_e32 v182, v185
	v_pk_fma_f32 v[6:7], v[184:185], v[108:109], v[6:7] op_sel_hi:[0,1,1]
	v_pk_fma_f32 v[6:7], v[182:183], v[110:111], v[6:7] op_sel_hi:[0,1,1]
	ds_read_b128 v[182:185], v210 offset:24816
	s_waitcnt lgkmcnt(1)
	v_pk_fma_f32 v[6:7], v[186:187], v[112:113], v[6:7] op_sel_hi:[0,1,1]
	v_pk_fma_f32 v[6:7], v[186:187], v[114:115], v[6:7] op_sel:[1,0,0]
	v_mov_b32_e32 v186, v189
	v_pk_fma_f32 v[6:7], v[188:189], v[116:117], v[6:7] op_sel_hi:[0,1,1]
	v_pk_fma_f32 v[6:7], v[186:187], v[118:119], v[6:7] op_sel_hi:[0,1,1]
	ds_read_b128 v[186:189], v210 offset:24832
	s_waitcnt lgkmcnt(1)
	v_pk_fma_f32 v[6:7], v[182:183], v[120:121], v[6:7] op_sel_hi:[0,1,1]
	v_pk_fma_f32 v[6:7], v[182:183], v[122:123], v[6:7] op_sel:[1,0,0]
	v_mov_b32_e32 v182, v185
	v_pk_fma_f32 v[6:7], v[184:185], v[124:125], v[6:7] op_sel_hi:[0,1,1]
	v_pk_fma_f32 v[6:7], v[182:183], v[126:127], v[6:7] op_sel_hi:[0,1,1]
	s_waitcnt lgkmcnt(0)
	v_pk_fma_f32 v[6:7], v[186:187], v[128:129], v[6:7] op_sel_hi:[0,1,1]
	v_pk_fma_f32 v[6:7], v[186:187], v[130:131], v[6:7] op_sel:[1,0,0]
	v_mov_b32_e32 v182, v189
	v_pk_fma_f32 v[6:7], v[188:189], v[132:133], v[6:7] op_sel_hi:[0,1,1]
	v_pk_fma_f32 v[6:7], v[182:183], v[134:135], v[6:7] op_sel_hi:[0,1,1]
	ds_read_b128 v[182:185], v210 offset:32784
	ds_read_b128 v[186:189], v210 offset:32800
	ds_read_b128 v[192:195], v210 offset:32816
	ds_read_b128 v[196:199], v210 offset:32832
	s_waitcnt lgkmcnt(3)
	v_pk_fma_f32 v[190:191], v[182:183], v[8:9], 0 op_sel_hi:[0,1,0]
	v_pk_fma_f32 v[182:183], v[182:183], v[10:11], v[190:191] op_sel:[1,0,0]
	v_mov_b32_e32 v222, v185
	v_pk_fma_f32 v[182:183], v[184:185], v[12:13], v[182:183] op_sel_hi:[0,1,1]
	v_pk_fma_f32 v[182:183], v[222:223], v[14:15], v[182:183] op_sel_hi:[0,1,1]
	s_waitcnt lgkmcnt(2)
	v_pk_fma_f32 v[182:183], v[186:187], v[16:17], v[182:183] op_sel_hi:[0,1,1]
	v_pk_fma_f32 v[182:183], v[186:187], v[18:19], v[182:183] op_sel:[1,0,0]
	v_mov_b32_e32 v184, v189
	v_pk_fma_f32 v[182:183], v[188:189], v[20:21], v[182:183] op_sel_hi:[0,1,1]
	v_pk_fma_f32 v[182:183], v[184:185], v[22:23], v[182:183] op_sel_hi:[0,1,1]
	s_waitcnt lgkmcnt(1)
; template <bool DRY = false>
; DI void phase_ln_router(const Params& p, char* smem, int bid, int nb) {
;     ...
;       f32x2_t acc[8];
; #pragma unroll
;       for (int j = 0; j < 8; ++j) acc[j] = (f32x2_t){0.f, 0.f};
; #pragma unroll
;       for (int j = 0; j < 8; ++j) {
; #pragma unroll
;         for (int i4 = 0; i4 < 16; ++i4) {
;           const float4 h = *(const float4*)(hs + j * 2048 + ks * 64 + 4 * i4);
;           acc[j] = __builtin_elementwise_fma((f32x2_t){h.x, h.x}, wr[4 * i4], acc[j]); acc[j] = __builtin_elementwise_fma((f32x2_t){h.y, h.y}, wr[4 * i4 + 1], acc[j]);
;           acc[j] = __builtin_elementwise_fma((f32x2_t){h.z, h.z}, wr[4 * i4 + 2], acc[j]); acc[j] = __builtin_elementwise_fma((f32x2_t){h.w, h.w}, wr[4 * i4 + 3], acc[j]);
;           if ((i4 & 7) == 7) __builtin_amdgcn_sched_barrier(0);
;         }
;       }
	v_pk_fma_f32 v[182:183], v[192:193], v[24:25], v[182:183] op_sel_hi:[0,1,1]
	v_pk_fma_f32 v[182:183], v[192:193], v[26:27], v[182:183] op_sel:[1,0,0]
	v_mov_b32_e32 v184, v195
	v_pk_fma_f32 v[182:183], v[194:195], v[28:29], v[182:183] op_sel_hi:[0,1,1]
	v_pk_fma_f32 v[182:183], v[184:185], v[30:31], v[182:183] op_sel_hi:[0,1,1]
	s_waitcnt lgkmcnt(0)
	v_pk_fma_f32 v[182:183], v[196:197], v[32:33], v[182:183] op_sel_hi:[0,1,1]
	v_pk_fma_f32 v[186:187], v[196:197], v[34:35], v[182:183] op_sel:[1,0,0]
	ds_read_b128 v[182:185], v210 offset:32848
	v_pk_fma_f32 v[186:187], v[198:199], v[36:37], v[186:187] op_sel_hi:[0,1,1]
	v_mov_b32_e32 v188, v199
	v_pk_fma_f32 v[190:191], v[188:189], v[38:39], v[186:187] op_sel_hi:[0,1,1]
	ds_read_b128 v[186:189], v210 offset:32864
	s_waitcnt lgkmcnt(1)
	v_pk_fma_f32 v[190:191], v[182:183], v[40:41], v[190:191] op_sel_hi:[0,1,1]
	v_pk_fma_f32 v[182:183], v[182:183], v[42:43], v[190:191] op_sel:[1,0,0]
	s_nop 0
	v_pk_fma_f32 v[182:183], v[184:185], v[44:45], v[182:183] op_sel_hi:[0,1,1]
	v_mov_b32_e32 v184, v185
	v_pk_fma_f32 v[182:183], v[184:185], v[46:47], v[182:183] op_sel_hi:[0,1,1]
	s_waitcnt lgkmcnt(0)
	v_pk_fma_f32 v[182:183], v[186:187], v[48:49], v[182:183] op_sel_hi:[0,1,1]
	v_pk_fma_f32 v[186:187], v[186:187], v[50:51], v[182:183] op_sel:[1,0,0]
	ds_read_b128 v[182:185], v210 offset:32880
	v_pk_fma_f32 v[186:187], v[188:189], v[52:53], v[186:187] op_sel_hi:[0,1,1]
	v_mov_b32_e32 v188, v189
	v_pk_fma_f32 v[190:191], v[188:189], v[54:55], v[186:187] op_sel_hi:[0,1,1]
	ds_read_b128 v[186:189], v210 offset:32896
	s_waitcnt lgkmcnt(1)
	v_pk_fma_f32 v[190:191], v[182:183], v[56:57], v[190:191] op_sel_hi:[0,1,1]
	v_pk_fma_f32 v[182:183], v[182:183], v[58:59], v[190:191] op_sel:[1,0,0]
	s_nop 0
	v_pk_fma_f32 v[182:183], v[184:185], v[60:61], v[182:183] op_sel_hi:[0,1,1]
	v_mov_b32_e32 v184, v185
	v_pk_fma_f32 v[182:183], v[184:185], v[62:63], v[182:183] op_sel_hi:[0,1,1]
	s_waitcnt lgkmcnt(0)
	v_pk_fma_f32 v[182:183], v[186:187], v[64:65], v[182:183] op_sel_hi:[0,1,1]
	v_pk_fma_f32 v[182:183], v[186:187], v[66:67], v[182:183] op_sel:[1,0,0]
	v_mov_b32_e32 v184, v189
	v_pk_fma_f32 v[182:183], v[188:189], v[68:69], v[182:183] op_sel_hi:[0,1,1]
	v_pk_fma_f32 v[190:191], v[184:185], v[70:71], v[182:183] op_sel_hi:[0,1,1]
	ds_read_b128 v[182:185], v210 offset:32912
	ds_read_b128 v[186:189], v210 offset:32928
	ds_read_b128 v[192:195], v210 offset:32944
	ds_read_b128 v[196:199], v210 offset:32960
	s_waitcnt lgkmcnt(3)
	v_pk_fma_f32 v[190:191], v[182:183], v[72:73], v[190:191] op_sel_hi:[0,1,1]
	v_pk_fma_f32 v[182:183], v[182:183], v[74:75], v[190:191] op_sel:[1,0,0]
	v_mov_b32_e32 v222, v185
	v_pk_fma_f32 v[182:183], v[184:185], v[76:77], v[182:183] op_sel_hi:[0,1,1]
	v_pk_fma_f32 v[182:183], v[222:223], v[78:79], v[182:183] op_sel_hi:[0,1,1]
	s_waitcnt lgkmcnt(2)
	v_pk_fma_f32 v[182:183], v[186:187], v[80:81], v[182:183] op_sel_hi:[0,1,1]
	v_pk_fma_f32 v[182:183], v[186:187], v[82:83], v[182:183] op_sel:[1,0,0]
	v_mov_b32_e32 v184, v189
	v_pk_fma_f32 v[182:183], v[188:189], v[84:85], v[182:183] op_sel_hi:[0,1,1]
	v_pk_fma_f32 v[182:183], v[184:185], v[86:87], v[182:183] op_sel_hi:[0,1,1]
	s_waitcnt lgkmcnt(1)
	v_pk_fma_f32 v[182:183], v[192:193], v[88:89], v[182:183] op_sel_hi:[0,1,1]
	v_pk_fma_f32 v[182:183], v[192:193], v[90:91], v[182:183] op_sel:[1,0,0]
	v_mov_b32_e32 v184, v195
	v_pk_fma_f32 v[182:183], v[194:195], v[92:93], v[182:183] op_sel_hi:[0,1,1]
	v_pk_fma_f32 v[182:183], v[184:185], v[94:95], v[182:183] op_sel_hi:[0,1,1]
	s_waitcnt lgkmcnt(0)
	v_pk_fma_f32 v[182:183], v[196:197], v[96:97], v[182:183] op_sel_hi:[0,1,1]
	v_pk_fma_f32 v[186:187], v[196:197], v[98:99], v[182:183] op_sel:[1,0,0]
	ds_read_b128 v[182:185], v210 offset:32976
	v_pk_fma_f32 v[186:187], v[198:199], v[100:101], v[186:187] op_sel_hi:[0,1,1]
	v_mov_b32_e32 v188, v199
	v_pk_fma_f32 v[190:191], v[188:189], v[102:103], v[186:187] op_sel_hi:[0,1,1]
	ds_read_b128 v[186:189], v210 offset:32992
	s_waitcnt lgkmcnt(1)
	v_pk_fma_f32 v[190:191], v[182:183], v[104:105], v[190:191] op_sel_hi:[0,1,1]
	v_pk_fma_f32 v[182:183], v[182:183], v[106:107], v[190:191] op_sel:[1,0,0]
	s_nop 0
	v_pk_fma_f32 v[182:183], v[184:185], v[108:109], v[182:183] op_sel_hi:[0,1,1]
	v_mov_b32_e32 v184, v185
	v_pk_fma_f32 v[182:183], v[184:185], v[110:111], v[182:183] op_sel_hi:[0,1,1]
	s_waitcnt lgkmcnt(0)
	v_pk_fma_f32 v[182:183], v[186:187], v[112:113], v[182:183] op_sel_hi:[0,1,1]
	v_pk_fma_f32 v[186:187], v[186:187], v[114:115], v[182:183] op_sel:[1,0,0]
	ds_read_b128 v[182:185], v210 offset:33008
	v_pk_fma_f32 v[186:187], v[188:189], v[116:117], v[186:187] op_sel_hi:[0,1,1]
	v_mov_b32_e32 v188, v189
	v_pk_fma_f32 v[190:191], v[188:189], v[118:119], v[186:187] op_sel_hi:[0,1,1]
	ds_read_b128 v[186:189], v210 offset:33024
	s_waitcnt lgkmcnt(1)
	v_pk_fma_f32 v[190:191], v[182:183], v[120:121], v[190:191] op_sel_hi:[0,1,1]
	v_pk_fma_f32 v[182:183], v[182:183], v[122:123], v[190:191] op_sel:[1,0,0]
	s_nop 0
	v_pk_fma_f32 v[182:183], v[184:185], v[124:125], v[182:183] op_sel_hi:[0,1,1]
	v_mov_b32_e32 v184, v185
	v_pk_fma_f32 v[182:183], v[184:185], v[126:127], v[182:183] op_sel_hi:[0,1,1]
	s_waitcnt lgkmcnt(0)
	v_pk_fma_f32 v[182:183], v[186:187], v[128:129], v[182:183] op_sel_hi:[0,1,1]
	v_pk_fma_f32 v[182:183], v[186:187], v[130:131], v[182:183] op_sel:[1,0,0]
	v_mov_b32_e32 v184, v189
	v_pk_fma_f32 v[182:183], v[188:189], v[132:133], v[182:183] op_sel_hi:[0,1,1]
	v_pk_fma_f32 v[182:183], v[184:185], v[134:135], v[182:183] op_sel_hi:[0,1,1]
	ds_read_b128 v[184:187], v210 offset:40976
	ds_read_b128 v[192:195], v210 offset:40992
	ds_read_b128 v[196:199], v210 offset:41008
	ds_read_b128 v[222:225], v210 offset:41024
	s_waitcnt lgkmcnt(3)
; template <bool DRY = false>
; DI void phase_ln_router(const Params& p, char* smem, int bid, int nb) {
;     ...
;       f32x2_t acc[8];
; #pragma unroll
;       for (int j = 0; j < 8; ++j) acc[j] = (f32x2_t){0.f, 0.f};
; #pragma unroll
;       for (int j = 0; j < 8; ++j) {
; #pragma unroll
;         for (int i4 = 0; i4 < 16; ++i4) {
;           const float4 h = *(const float4*)(hs + j * 2048 + ks * 64 + 4 * i4);
;           acc[j] = __builtin_elementwise_fma((f32x2_t){h.x, h.x}, wr[4 * i4], acc[j]); acc[j] = __builtin_elementwise_fma((f32x2_t){h.y, h.y}, wr[4 * i4 + 1], acc[j]);
;           acc[j] = __builtin_elementwise_fma((f32x2_t){h.z, h.z}, wr[4 * i4 + 2], acc[j]); acc[j] = __builtin_elementwise_fma((f32x2_t){h.w, h.w}, wr[4 * i4 + 3], acc[j]);
;           if ((i4 & 7) == 7) __builtin_amdgcn_sched_barrier(0);
;         }
;       }
	v_pk_fma_f32 v[188:189], v[184:185], v[8:9], 0 op_sel_hi:[0,1,0]
	v_pk_fma_f32 v[184:185], v[184:185], v[10:11], v[188:189] op_sel:[1,0,0]
	v_mov_b32_e32 v190, v187
	v_pk_fma_f32 v[184:185], v[186:187], v[12:13], v[184:185] op_sel_hi:[0,1,1]
	v_pk_fma_f32 v[184:185], v[190:191], v[14:15], v[184:185] op_sel_hi:[0,1,1]
	s_waitcnt lgkmcnt(2)
	v_pk_fma_f32 v[184:185], v[192:193], v[16:17], v[184:185] op_sel_hi:[0,1,1]
	v_pk_fma_f32 v[184:185], v[192:193], v[18:19], v[184:185] op_sel:[1,0,0]
	v_mov_b32_e32 v186, v195
	v_pk_fma_f32 v[184:185], v[194:195], v[20:21], v[184:185] op_sel_hi:[0,1,1]
	v_pk_fma_f32 v[184:185], v[186:187], v[22:23], v[184:185] op_sel_hi:[0,1,1]
	s_waitcnt lgkmcnt(1)
	v_pk_fma_f32 v[184:185], v[196:197], v[24:25], v[184:185] op_sel_hi:[0,1,1]
	v_pk_fma_f32 v[184:185], v[196:197], v[26:27], v[184:185] op_sel:[1,0,0]
	v_mov_b32_e32 v186, v199
	v_pk_fma_f32 v[184:185], v[198:199], v[28:29], v[184:185] op_sel_hi:[0,1,1]
	v_pk_fma_f32 v[184:185], v[186:187], v[30:31], v[184:185] op_sel_hi:[0,1,1]
	s_waitcnt lgkmcnt(0)
	v_pk_fma_f32 v[184:185], v[222:223], v[32:33], v[184:185] op_sel_hi:[0,1,1]
	v_pk_fma_f32 v[188:189], v[222:223], v[34:35], v[184:185] op_sel:[1,0,0]
	ds_read_b128 v[184:187], v210 offset:41040
	ds_read_b128 v[192:195], v210 offset:41056
	v_pk_fma_f32 v[188:189], v[224:225], v[36:37], v[188:189] op_sel_hi:[0,1,1]
	v_mov_b32_e32 v190, v225
	v_pk_fma_f32 v[188:189], v[190:191], v[38:39], v[188:189] op_sel_hi:[0,1,1]
	s_waitcnt lgkmcnt(1)
	v_pk_fma_f32 v[188:189], v[184:185], v[40:41], v[188:189] op_sel_hi:[0,1,1]
	v_pk_fma_f32 v[184:185], v[184:185], v[42:43], v[188:189] op_sel:[1,0,0]
	s_waitcnt lgkmcnt(0)
	v_mov_b32_e32 v190, v195
	v_pk_fma_f32 v[184:185], v[186:187], v[44:45], v[184:185] op_sel_hi:[0,1,1]
	v_mov_b32_e32 v186, v187
	v_pk_fma_f32 v[184:185], v[186:187], v[46:47], v[184:185] op_sel_hi:[0,1,1]
	v_pk_fma_f32 v[184:185], v[192:193], v[48:49], v[184:185] op_sel_hi:[0,1,1]
	v_pk_fma_f32 v[188:189], v[192:193], v[50:51], v[184:185] op_sel:[1,0,0]
	ds_read_b128 v[184:187], v210 offset:41072
	v_pk_fma_f32 v[188:189], v[194:195], v[52:53], v[188:189] op_sel_hi:[0,1,1]
	v_pk_fma_f32 v[188:189], v[190:191], v[54:55], v[188:189] op_sel_hi:[0,1,1]
	ds_read_b128 v[192:195], v210 offset:41088
	s_waitcnt lgkmcnt(1)
	v_pk_fma_f32 v[188:189], v[184:185], v[56:57], v[188:189] op_sel_hi:[0,1,1]
	v_pk_fma_f32 v[184:185], v[184:185], v[58:59], v[188:189] op_sel:[1,0,0]
	s_nop 0
	v_pk_fma_f32 v[184:185], v[186:187], v[60:61], v[184:185] op_sel_hi:[0,1,1]
	v_mov_b32_e32 v186, v187
	v_pk_fma_f32 v[184:185], v[186:187], v[62:63], v[184:185] op_sel_hi:[0,1,1]
	s_waitcnt lgkmcnt(0)
	v_pk_fma_f32 v[184:185], v[192:193], v[64:65], v[184:185] op_sel_hi:[0,1,1]
	v_pk_fma_f32 v[184:185], v[192:193], v[66:67], v[184:185] op_sel:[1,0,0]
	v_mov_b32_e32 v186, v195
	v_pk_fma_f32 v[184:185], v[194:195], v[68:69], v[184:185] op_sel_hi:[0,1,1]
	v_pk_fma_f32 v[188:189], v[186:187], v[70:71], v[184:185] op_sel_hi:[0,1,1]
	ds_read_b128 v[184:187], v210 offset:41104
	ds_read_b128 v[192:195], v210 offset:41120
	ds_read_b128 v[196:199], v210 offset:41136
	ds_read_b128 v[222:225], v210 offset:41152
	s_waitcnt lgkmcnt(3)
	v_pk_fma_f32 v[188:189], v[184:185], v[72:73], v[188:189] op_sel_hi:[0,1,1]
	v_pk_fma_f32 v[184:185], v[184:185], v[74:75], v[188:189] op_sel:[1,0,0]
	v_mov_b32_e32 v190, v187
	v_pk_fma_f32 v[184:185], v[186:187], v[76:77], v[184:185] op_sel_hi:[0,1,1]
	v_pk_fma_f32 v[184:185], v[190:191], v[78:79], v[184:185] op_sel_hi:[0,1,1]
	s_waitcnt lgkmcnt(2)
	v_pk_fma_f32 v[184:185], v[192:193], v[80:81], v[184:185] op_sel_hi:[0,1,1]
	v_pk_fma_f32 v[184:185], v[192:193], v[82:83], v[184:185] op_sel:[1,0,0]
	v_mov_b32_e32 v186, v195
	v_pk_fma_f32 v[184:185], v[194:195], v[84:85], v[184:185] op_sel_hi:[0,1,1]
	v_pk_fma_f32 v[184:185], v[186:187], v[86:87], v[184:185] op_sel_hi:[0,1,1]
	s_waitcnt lgkmcnt(1)
	v_pk_fma_f32 v[184:185], v[196:197], v[88:89], v[184:185] op_sel_hi:[0,1,1]
	v_pk_fma_f32 v[184:185], v[196:197], v[90:91], v[184:185] op_sel:[1,0,0]
	v_mov_b32_e32 v186, v199
	v_pk_fma_f32 v[184:185], v[198:199], v[92:93], v[184:185] op_sel_hi:[0,1,1]
	v_pk_fma_f32 v[184:185], v[186:187], v[94:95], v[184:185] op_sel_hi:[0,1,1]
	s_waitcnt lgkmcnt(0)
	v_pk_fma_f32 v[184:185], v[222:223], v[96:97], v[184:185] op_sel_hi:[0,1,1]
	v_pk_fma_f32 v[188:189], v[222:223], v[98:99], v[184:185] op_sel:[1,0,0]
	ds_read_b128 v[184:187], v210 offset:41168
	ds_read_b128 v[192:195], v210 offset:41184
	v_pk_fma_f32 v[188:189], v[224:225], v[100:101], v[188:189] op_sel_hi:[0,1,1]
	v_mov_b32_e32 v190, v225
	v_pk_fma_f32 v[188:189], v[190:191], v[102:103], v[188:189] op_sel_hi:[0,1,1]
	s_waitcnt lgkmcnt(1)
	v_pk_fma_f32 v[188:189], v[184:185], v[104:105], v[188:189] op_sel_hi:[0,1,1]
	v_pk_fma_f32 v[184:185], v[184:185], v[106:107], v[188:189] op_sel:[1,0,0]
	s_waitcnt lgkmcnt(0)
	v_mov_b32_e32 v190, v195
	v_pk_fma_f32 v[184:185], v[186:187], v[108:109], v[184:185] op_sel_hi:[0,1,1]
	v_mov_b32_e32 v186, v187
	v_pk_fma_f32 v[184:185], v[186:187], v[110:111], v[184:185] op_sel_hi:[0,1,1]
	v_pk_fma_f32 v[184:185], v[192:193], v[112:113], v[184:185] op_sel_hi:[0,1,1]
	v_pk_fma_f32 v[188:189], v[192:193], v[114:115], v[184:185] op_sel:[1,0,0]
	ds_read_b128 v[184:187], v210 offset:41200
	v_pk_fma_f32 v[188:189], v[194:195], v[116:117], v[188:189] op_sel_hi:[0,1,1]
	v_pk_fma_f32 v[188:189], v[190:191], v[118:119], v[188:189] op_sel_hi:[0,1,1]
	ds_read_b128 v[192:195], v210 offset:41216
	s_waitcnt lgkmcnt(1)
; template <bool DRY = false>
; DI void phase_ln_router(const Params& p, char* smem, int bid, int nb) {
;     ...
;       f32x2_t acc[8];
; #pragma unroll
;       for (int j = 0; j < 8; ++j) acc[j] = (f32x2_t){0.f, 0.f};
; #pragma unroll
;       for (int j = 0; j < 8; ++j) {
; #pragma unroll
;         for (int i4 = 0; i4 < 16; ++i4) {
;           const float4 h = *(const float4*)(hs + j * 2048 + ks * 64 + 4 * i4);
;           acc[j] = __builtin_elementwise_fma((f32x2_t){h.x, h.x}, wr[4 * i4], acc[j]); acc[j] = __builtin_elementwise_fma((f32x2_t){h.y, h.y}, wr[4 * i4 + 1], acc[j]);
;           acc[j] = __builtin_elementwise_fma((f32x2_t){h.z, h.z}, wr[4 * i4 + 2], acc[j]); acc[j] = __builtin_elementwise_fma((f32x2_t){h.w, h.w}, wr[4 * i4 + 3], acc[j]);
;           if ((i4 & 7) == 7) __builtin_amdgcn_sched_barrier(0);
;         }
;       }
	v_pk_fma_f32 v[188:189], v[184:185], v[120:121], v[188:189] op_sel_hi:[0,1,1]
	v_pk_fma_f32 v[184:185], v[184:185], v[122:123], v[188:189] op_sel:[1,0,0]
	s_nop 0
	v_pk_fma_f32 v[184:185], v[186:187], v[124:125], v[184:185] op_sel_hi:[0,1,1]
	v_mov_b32_e32 v186, v187
	v_pk_fma_f32 v[184:185], v[186:187], v[126:127], v[184:185] op_sel_hi:[0,1,1]
	s_waitcnt lgkmcnt(0)
	v_pk_fma_f32 v[184:185], v[192:193], v[128:129], v[184:185] op_sel_hi:[0,1,1]
	v_pk_fma_f32 v[184:185], v[192:193], v[130:131], v[184:185] op_sel:[1,0,0]
	v_mov_b32_e32 v186, v195
	v_pk_fma_f32 v[184:185], v[194:195], v[132:133], v[184:185] op_sel_hi:[0,1,1]
	v_pk_fma_f32 v[184:185], v[186:187], v[134:135], v[184:185] op_sel_hi:[0,1,1]
	ds_read_b128 v[186:189], v210 offset:49168
	ds_read_b128 v[192:195], v210 offset:49184
	ds_read_b128 v[196:199], v210 offset:49200
	ds_read_b128 v[222:225], v210 offset:49216
	s_waitcnt lgkmcnt(3)
	v_pk_fma_f32 v[190:191], v[186:187], v[8:9], 0 op_sel_hi:[0,1,0]
	v_pk_fma_f32 v[186:187], v[186:187], v[10:11], v[190:191] op_sel:[1,0,0]
	v_mov_b32_e32 v226, v189
	v_pk_fma_f32 v[186:187], v[188:189], v[12:13], v[186:187] op_sel_hi:[0,1,1]
	v_pk_fma_f32 v[186:187], v[226:227], v[14:15], v[186:187] op_sel_hi:[0,1,1]
	s_waitcnt lgkmcnt(2)
	v_pk_fma_f32 v[186:187], v[192:193], v[16:17], v[186:187] op_sel_hi:[0,1,1]
	v_pk_fma_f32 v[186:187], v[192:193], v[18:19], v[186:187] op_sel:[1,0,0]
	v_mov_b32_e32 v188, v195
	v_pk_fma_f32 v[186:187], v[194:195], v[20:21], v[186:187] op_sel_hi:[0,1,1]
	v_pk_fma_f32 v[186:187], v[188:189], v[22:23], v[186:187] op_sel_hi:[0,1,1]
	s_waitcnt lgkmcnt(1)
	v_pk_fma_f32 v[186:187], v[196:197], v[24:25], v[186:187] op_sel_hi:[0,1,1]
	v_pk_fma_f32 v[186:187], v[196:197], v[26:27], v[186:187] op_sel:[1,0,0]
	v_mov_b32_e32 v188, v199
	v_pk_fma_f32 v[186:187], v[198:199], v[28:29], v[186:187] op_sel_hi:[0,1,1]
	v_pk_fma_f32 v[186:187], v[188:189], v[30:31], v[186:187] op_sel_hi:[0,1,1]
	s_waitcnt lgkmcnt(0)
	v_pk_fma_f32 v[186:187], v[222:223], v[32:33], v[186:187] op_sel_hi:[0,1,1]
	v_pk_fma_f32 v[190:191], v[222:223], v[34:35], v[186:187] op_sel:[1,0,0]
	ds_read_b128 v[186:189], v210 offset:49232
	v_pk_fma_f32 v[190:191], v[224:225], v[36:37], v[190:191] op_sel_hi:[0,1,1]
	v_mov_b32_e32 v192, v225
	v_pk_fma_f32 v[190:191], v[192:193], v[38:39], v[190:191] op_sel_hi:[0,1,1]
	ds_read_b128 v[192:195], v210 offset:49248
	s_waitcnt lgkmcnt(1)
	v_pk_fma_f32 v[190:191], v[186:187], v[40:41], v[190:191] op_sel_hi:[0,1,1]
	v_pk_fma_f32 v[186:187], v[186:187], v[42:43], v[190:191] op_sel:[1,0,0]
	s_nop 0
	v_pk_fma_f32 v[186:187], v[188:189], v[44:45], v[186:187] op_sel_hi:[0,1,1]
	v_mov_b32_e32 v188, v189
	v_pk_fma_f32 v[186:187], v[188:189], v[46:47], v[186:187] op_sel_hi:[0,1,1]
	s_waitcnt lgkmcnt(0)
	v_pk_fma_f32 v[186:187], v[192:193], v[48:49], v[186:187] op_sel_hi:[0,1,1]
	v_pk_fma_f32 v[190:191], v[192:193], v[50:51], v[186:187] op_sel:[1,0,0]
	ds_read_b128 v[186:189], v210 offset:49264
	v_pk_fma_f32 v[190:191], v[194:195], v[52:53], v[190:191] op_sel_hi:[0,1,1]
	v_mov_b32_e32 v192, v195
	v_pk_fma_f32 v[190:191], v[192:193], v[54:55], v[190:191] op_sel_hi:[0,1,1]
	ds_read_b128 v[192:195], v210 offset:49280
	s_waitcnt lgkmcnt(1)
	v_pk_fma_f32 v[190:191], v[186:187], v[56:57], v[190:191] op_sel_hi:[0,1,1]
	v_pk_fma_f32 v[186:187], v[186:187], v[58:59], v[190:191] op_sel:[1,0,0]
	s_nop 0
	v_pk_fma_f32 v[186:187], v[188:189], v[60:61], v[186:187] op_sel_hi:[0,1,1]
	v_mov_b32_e32 v188, v189
	v_pk_fma_f32 v[186:187], v[188:189], v[62:63], v[186:187] op_sel_hi:[0,1,1]
	s_waitcnt lgkmcnt(0)
	v_pk_fma_f32 v[186:187], v[192:193], v[64:65], v[186:187] op_sel_hi:[0,1,1]
	v_pk_fma_f32 v[186:187], v[192:193], v[66:67], v[186:187] op_sel:[1,0,0]
	v_mov_b32_e32 v188, v195
	v_pk_fma_f32 v[186:187], v[194:195], v[68:69], v[186:187] op_sel_hi:[0,1,1]
	v_pk_fma_f32 v[190:191], v[188:189], v[70:71], v[186:187] op_sel_hi:[0,1,1]
	ds_read_b128 v[186:189], v210 offset:49296
	ds_read_b128 v[192:195], v210 offset:49312
	ds_read_b128 v[196:199], v210 offset:49328
	ds_read_b128 v[222:225], v210 offset:49344
	s_waitcnt lgkmcnt(3)
	v_pk_fma_f32 v[190:191], v[186:187], v[72:73], v[190:191] op_sel_hi:[0,1,1]
	v_pk_fma_f32 v[186:187], v[186:187], v[74:75], v[190:191] op_sel:[1,0,0]
	v_mov_b32_e32 v226, v189
	v_pk_fma_f32 v[186:187], v[188:189], v[76:77], v[186:187] op_sel_hi:[0,1,1]
	v_pk_fma_f32 v[186:187], v[226:227], v[78:79], v[186:187] op_sel_hi:[0,1,1]
	s_waitcnt lgkmcnt(2)
	v_pk_fma_f32 v[186:187], v[192:193], v[80:81], v[186:187] op_sel_hi:[0,1,1]
	v_pk_fma_f32 v[186:187], v[192:193], v[82:83], v[186:187] op_sel:[1,0,0]
	v_mov_b32_e32 v188, v195
	v_pk_fma_f32 v[186:187], v[194:195], v[84:85], v[186:187] op_sel_hi:[0,1,1]
	v_pk_fma_f32 v[186:187], v[188:189], v[86:87], v[186:187] op_sel_hi:[0,1,1]
	s_waitcnt lgkmcnt(1)
	v_pk_fma_f32 v[186:187], v[196:197], v[88:89], v[186:187] op_sel_hi:[0,1,1]
	v_pk_fma_f32 v[186:187], v[196:197], v[90:91], v[186:187] op_sel:[1,0,0]
	v_mov_b32_e32 v188, v199
	v_pk_fma_f32 v[186:187], v[198:199], v[92:93], v[186:187] op_sel_hi:[0,1,1]
	v_pk_fma_f32 v[186:187], v[188:189], v[94:95], v[186:187] op_sel_hi:[0,1,1]
	s_waitcnt lgkmcnt(0)
	v_pk_fma_f32 v[186:187], v[222:223], v[96:97], v[186:187] op_sel_hi:[0,1,1]
	v_pk_fma_f32 v[190:191], v[222:223], v[98:99], v[186:187] op_sel:[1,0,0]
	ds_read_b128 v[186:189], v210 offset:49360
	v_pk_fma_f32 v[190:191], v[224:225], v[100:101], v[190:191] op_sel_hi:[0,1,1]
	v_mov_b32_e32 v192, v225
	v_pk_fma_f32 v[190:191], v[192:193], v[102:103], v[190:191] op_sel_hi:[0,1,1]
	ds_read_b128 v[192:195], v210 offset:49376
	s_waitcnt lgkmcnt(1)
; template <bool DRY = false>
; DI void phase_ln_router(const Params& p, char* smem, int bid, int nb) {
;     ...
;       f32x2_t acc[8];
; #pragma unroll
;       for (int j = 0; j < 8; ++j) acc[j] = (f32x2_t){0.f, 0.f};
; #pragma unroll
;       for (int j = 0; j < 8; ++j) {
; #pragma unroll
;         for (int i4 = 0; i4 < 16; ++i4) {
;           const float4 h = *(const float4*)(hs + j * 2048 + ks * 64 + 4 * i4);
;           acc[j] = __builtin_elementwise_fma((f32x2_t){h.x, h.x}, wr[4 * i4], acc[j]); acc[j] = __builtin_elementwise_fma((f32x2_t){h.y, h.y}, wr[4 * i4 + 1], acc[j]);
;           acc[j] = __builtin_elementwise_fma((f32x2_t){h.z, h.z}, wr[4 * i4 + 2], acc[j]); acc[j] = __builtin_elementwise_fma((f32x2_t){h.w, h.w}, wr[4 * i4 + 3], acc[j]);
;           if ((i4 & 7) == 7) __builtin_amdgcn_sched_barrier(0);
;         }
;       }
	v_pk_fma_f32 v[190:191], v[186:187], v[104:105], v[190:191] op_sel_hi:[0,1,1]
	v_pk_fma_f32 v[186:187], v[186:187], v[106:107], v[190:191] op_sel:[1,0,0]
	s_nop 0
	v_pk_fma_f32 v[186:187], v[188:189], v[108:109], v[186:187] op_sel_hi:[0,1,1]
	v_mov_b32_e32 v188, v189
	v_pk_fma_f32 v[186:187], v[188:189], v[110:111], v[186:187] op_sel_hi:[0,1,1]
	s_waitcnt lgkmcnt(0)
	v_pk_fma_f32 v[186:187], v[192:193], v[112:113], v[186:187] op_sel_hi:[0,1,1]
	v_pk_fma_f32 v[190:191], v[192:193], v[114:115], v[186:187] op_sel:[1,0,0]
	ds_read_b128 v[186:189], v210 offset:49392
	v_pk_fma_f32 v[190:191], v[194:195], v[116:117], v[190:191] op_sel_hi:[0,1,1]
	v_mov_b32_e32 v192, v195
	v_pk_fma_f32 v[190:191], v[192:193], v[118:119], v[190:191] op_sel_hi:[0,1,1]
	ds_read_b128 v[192:195], v210 offset:49408
	s_waitcnt lgkmcnt(1)
	v_pk_fma_f32 v[190:191], v[186:187], v[120:121], v[190:191] op_sel_hi:[0,1,1]
	v_pk_fma_f32 v[186:187], v[186:187], v[122:123], v[190:191] op_sel:[1,0,0]
	s_nop 0
	v_pk_fma_f32 v[186:187], v[188:189], v[124:125], v[186:187] op_sel_hi:[0,1,1]
	v_mov_b32_e32 v188, v189
	v_pk_fma_f32 v[186:187], v[188:189], v[126:127], v[186:187] op_sel_hi:[0,1,1]
	s_waitcnt lgkmcnt(0)
	v_pk_fma_f32 v[186:187], v[192:193], v[128:129], v[186:187] op_sel_hi:[0,1,1]
	v_pk_fma_f32 v[186:187], v[192:193], v[130:131], v[186:187] op_sel:[1,0,0]
	v_mov_b32_e32 v188, v195
	v_pk_fma_f32 v[186:187], v[194:195], v[132:133], v[186:187] op_sel_hi:[0,1,1]
	v_pk_fma_f32 v[190:191], v[188:189], v[134:135], v[186:187] op_sel_hi:[0,1,1]
	ds_read_b128 v[186:189], v210 offset:57360
	ds_read_b128 v[192:195], v210 offset:57376
	ds_read_b128 v[196:199], v210 offset:57392
	ds_read_b128 v[222:225], v210 offset:57408
	s_waitcnt lgkmcnt(3)
	v_pk_fma_f32 v[226:227], v[186:187], v[8:9], 0 op_sel_hi:[0,1,0]
	v_pk_fma_f32 v[186:187], v[186:187], v[10:11], v[226:227] op_sel:[1,0,0]
	v_mov_b32_e32 v228, v189
	v_pk_fma_f32 v[186:187], v[188:189], v[12:13], v[186:187] op_sel_hi:[0,1,1]
	v_pk_fma_f32 v[186:187], v[228:229], v[14:15], v[186:187] op_sel_hi:[0,1,1]
	s_waitcnt lgkmcnt(2)
	v_pk_fma_f32 v[186:187], v[192:193], v[16:17], v[186:187] op_sel_hi:[0,1,1]
	v_pk_fma_f32 v[186:187], v[192:193], v[18:19], v[186:187] op_sel:[1,0,0]
	v_mov_b32_e32 v188, v195
	v_pk_fma_f32 v[186:187], v[194:195], v[20:21], v[186:187] op_sel_hi:[0,1,1]
	v_pk_fma_f32 v[186:187], v[188:189], v[22:23], v[186:187] op_sel_hi:[0,1,1]
	s_waitcnt lgkmcnt(1)
	v_pk_fma_f32 v[186:187], v[196:197], v[24:25], v[186:187] op_sel_hi:[0,1,1]
	v_pk_fma_f32 v[186:187], v[196:197], v[26:27], v[186:187] op_sel:[1,0,0]
	v_mov_b32_e32 v188, v199
	v_pk_fma_f32 v[186:187], v[198:199], v[28:29], v[186:187] op_sel_hi:[0,1,1]
	v_pk_fma_f32 v[186:187], v[188:189], v[30:31], v[186:187] op_sel_hi:[0,1,1]
	s_waitcnt lgkmcnt(0)
	v_pk_fma_f32 v[186:187], v[222:223], v[32:33], v[186:187] op_sel_hi:[0,1,1]
	v_pk_fma_f32 v[192:193], v[222:223], v[34:35], v[186:187] op_sel:[1,0,0]
	ds_read_b128 v[186:189], v210 offset:57424
	v_pk_fma_f32 v[192:193], v[224:225], v[36:37], v[192:193] op_sel_hi:[0,1,1]
	v_mov_b32_e32 v194, v225
	v_pk_fma_f32 v[196:197], v[194:195], v[38:39], v[192:193] op_sel_hi:[0,1,1]
	ds_read_b128 v[192:195], v210 offset:57440
	s_waitcnt lgkmcnt(1)
	v_pk_fma_f32 v[196:197], v[186:187], v[40:41], v[196:197] op_sel_hi:[0,1,1]
	v_pk_fma_f32 v[186:187], v[186:187], v[42:43], v[196:197] op_sel:[1,0,0]
	s_nop 0
	v_pk_fma_f32 v[186:187], v[188:189], v[44:45], v[186:187] op_sel_hi:[0,1,1]
	v_mov_b32_e32 v188, v189
	v_pk_fma_f32 v[186:187], v[188:189], v[46:47], v[186:187] op_sel_hi:[0,1,1]
	s_waitcnt lgkmcnt(0)
	v_pk_fma_f32 v[186:187], v[192:193], v[48:49], v[186:187] op_sel_hi:[0,1,1]
	v_pk_fma_f32 v[192:193], v[192:193], v[50:51], v[186:187] op_sel:[1,0,0]
	ds_read_b128 v[186:189], v210 offset:57456
	v_pk_fma_f32 v[192:193], v[194:195], v[52:53], v[192:193] op_sel_hi:[0,1,1]
	v_mov_b32_e32 v194, v195
	v_pk_fma_f32 v[196:197], v[194:195], v[54:55], v[192:193] op_sel_hi:[0,1,1]
	ds_read_b128 v[192:195], v210 offset:57472
	s_waitcnt lgkmcnt(1)
	v_pk_fma_f32 v[196:197], v[186:187], v[56:57], v[196:197] op_sel_hi:[0,1,1]
	v_pk_fma_f32 v[186:187], v[186:187], v[58:59], v[196:197] op_sel:[1,0,0]
	s_nop 0
	v_pk_fma_f32 v[186:187], v[188:189], v[60:61], v[186:187] op_sel_hi:[0,1,1]
	v_mov_b32_e32 v188, v189
	v_pk_fma_f32 v[186:187], v[188:189], v[62:63], v[186:187] op_sel_hi:[0,1,1]
	s_waitcnt lgkmcnt(0)
	v_pk_fma_f32 v[186:187], v[192:193], v[64:65], v[186:187] op_sel_hi:[0,1,1]
	v_pk_fma_f32 v[186:187], v[192:193], v[66:67], v[186:187] op_sel:[1,0,0]
	v_mov_b32_e32 v188, v195
	v_pk_fma_f32 v[186:187], v[194:195], v[68:69], v[186:187] op_sel_hi:[0,1,1]
	v_pk_fma_f32 v[226:227], v[188:189], v[70:71], v[186:187] op_sel_hi:[0,1,1]
	ds_read_b128 v[186:189], v210 offset:57488
	ds_read_b128 v[192:195], v210 offset:57504
	ds_read_b128 v[196:199], v210 offset:57520
	ds_read_b128 v[222:225], v210 offset:57536
	s_waitcnt lgkmcnt(3)
	v_pk_fma_f32 v[226:227], v[186:187], v[72:73], v[226:227] op_sel_hi:[0,1,1]
	v_pk_fma_f32 v[186:187], v[186:187], v[74:75], v[226:227] op_sel:[1,0,0]
	v_mov_b32_e32 v228, v189
	v_pk_fma_f32 v[186:187], v[188:189], v[76:77], v[186:187] op_sel_hi:[0,1,1]
	v_pk_fma_f32 v[186:187], v[228:229], v[78:79], v[186:187] op_sel_hi:[0,1,1]
	s_waitcnt lgkmcnt(2)
; template <bool DRY = false>
; DI void phase_ln_router(const Params& p, char* smem, int bid, int nb) {
;     ...
;       for (int j = 0; j < 8; ++j) {
; #pragma unroll
;         for (int i4 = 0; i4 < 16; ++i4) {
;           const float4 h = *(const float4*)(hs + j * 2048 + ks * 64 + 4 * i4);
;           acc[j] = __builtin_elementwise_fma((f32x2_t){h.x, h.x}, wr[4 * i4], acc[j]); acc[j] = __builtin_elementwise_fma((f32x2_t){h.y, h.y}, wr[4 * i4 + 1], acc[j]);
;           acc[j] = __builtin_elementwise_fma((f32x2_t){h.z, h.z}, wr[4 * i4 + 2], acc[j]); acc[j] = __builtin_elementwise_fma((f32x2_t){h.w, h.w}, wr[4 * i4 + 3], acc[j]);
;           if ((i4 & 7) == 7) __builtin_amdgcn_sched_barrier(0);
;         }
;       }
; #pragma unroll
;       for (int j = 0; j < 8; ++j) { red[(ks * 8 + j) * 32 + e] = acc[j][0]; red[(ks * 8 + j) * 32 + e + 16] = acc[j][1]; }
;     }
;     __syncthreads();
;     if (tid < 256) {
;       const int e2 = tid & 31, j = tid >> 5;
;       float s = 0.f;
; #pragma unroll
;       for (int k2 = 0; k2 < 32; ++k2) s += red[(k2 * 8 + j) * 32 + e2];
;       lg[j * 32 + e2] = s + p.b_router[e2];
	v_pk_fma_f32 v[186:187], v[192:193], v[80:81], v[186:187] op_sel_hi:[0,1,1]
	v_pk_fma_f32 v[186:187], v[192:193], v[82:83], v[186:187] op_sel:[1,0,0]
	v_mov_b32_e32 v188, v195
	v_pk_fma_f32 v[186:187], v[194:195], v[84:85], v[186:187] op_sel_hi:[0,1,1]
	v_pk_fma_f32 v[186:187], v[188:189], v[86:87], v[186:187] op_sel_hi:[0,1,1]
	s_waitcnt lgkmcnt(1)
	v_pk_fma_f32 v[186:187], v[196:197], v[88:89], v[186:187] op_sel_hi:[0,1,1]
	v_pk_fma_f32 v[186:187], v[196:197], v[90:91], v[186:187] op_sel:[1,0,0]
	v_mov_b32_e32 v188, v199
	v_pk_fma_f32 v[186:187], v[198:199], v[92:93], v[186:187] op_sel_hi:[0,1,1]
	v_pk_fma_f32 v[186:187], v[188:189], v[94:95], v[186:187] op_sel_hi:[0,1,1]
	s_waitcnt lgkmcnt(0)
	v_pk_fma_f32 v[186:187], v[222:223], v[96:97], v[186:187] op_sel_hi:[0,1,1]
	v_pk_fma_f32 v[192:193], v[222:223], v[98:99], v[186:187] op_sel:[1,0,0]
	ds_read_b128 v[186:189], v210 offset:57552
	v_pk_fma_f32 v[192:193], v[224:225], v[100:101], v[192:193] op_sel_hi:[0,1,1]
	v_mov_b32_e32 v194, v225
	v_pk_fma_f32 v[196:197], v[194:195], v[102:103], v[192:193] op_sel_hi:[0,1,1]
	ds_read_b128 v[192:195], v210 offset:57568
	s_waitcnt lgkmcnt(1)
	v_pk_fma_f32 v[196:197], v[186:187], v[104:105], v[196:197] op_sel_hi:[0,1,1]
	v_pk_fma_f32 v[186:187], v[186:187], v[106:107], v[196:197] op_sel:[1,0,0]
	s_nop 0
	v_pk_fma_f32 v[186:187], v[188:189], v[108:109], v[186:187] op_sel_hi:[0,1,1]
	v_mov_b32_e32 v188, v189
	v_pk_fma_f32 v[186:187], v[188:189], v[110:111], v[186:187] op_sel_hi:[0,1,1]
	s_waitcnt lgkmcnt(0)
	v_pk_fma_f32 v[186:187], v[192:193], v[112:113], v[186:187] op_sel_hi:[0,1,1]
	v_pk_fma_f32 v[192:193], v[192:193], v[114:115], v[186:187] op_sel:[1,0,0]
	ds_read_b128 v[186:189], v210 offset:57584
	v_pk_fma_f32 v[192:193], v[194:195], v[116:117], v[192:193] op_sel_hi:[0,1,1]
	v_mov_b32_e32 v194, v195
	v_pk_fma_f32 v[196:197], v[194:195], v[118:119], v[192:193] op_sel_hi:[0,1,1]
	ds_read_b128 v[192:195], v210 offset:57600
	s_waitcnt lgkmcnt(1)
	v_pk_fma_f32 v[196:197], v[186:187], v[120:121], v[196:197] op_sel_hi:[0,1,1]
	v_pk_fma_f32 v[186:187], v[186:187], v[122:123], v[196:197] op_sel:[1,0,0]
	s_nop 0
	v_pk_fma_f32 v[186:187], v[188:189], v[124:125], v[186:187] op_sel_hi:[0,1,1]
	v_mov_b32_e32 v188, v189
	v_pk_fma_f32 v[186:187], v[188:189], v[126:127], v[186:187] op_sel_hi:[0,1,1]
	s_waitcnt lgkmcnt(0)
	v_pk_fma_f32 v[186:187], v[192:193], v[128:129], v[186:187] op_sel_hi:[0,1,1]
	v_pk_fma_f32 v[186:187], v[192:193], v[130:131], v[186:187] op_sel:[1,0,0]
	v_mov_b32_e32 v188, v195
	v_pk_fma_f32 v[186:187], v[194:195], v[132:133], v[186:187] op_sel_hi:[0,1,1]
	v_pk_fma_f32 v[186:187], v[188:189], v[134:135], v[186:187] op_sel_hi:[0,1,1]
	ds_write2_b32 v217, v0, v1 offset1:16
	ds_write2_b32 v217, v2, v3 offset0:32 offset1:48
	ds_write2_b32 v217, v4, v5 offset0:64 offset1:80
	ds_write2_b32 v217, v6, v7 offset0:96 offset1:112
	ds_write2_b32 v217, v182, v183 offset0:128 offset1:144
	ds_write2_b32 v217, v184, v185 offset0:160 offset1:176
	ds_write2_b32 v217, v190, v191 offset0:192 offset1:208
	ds_write2_b32 v217, v186, v187 offset0:224 offset1:240
	s_waitcnt lgkmcnt(0)
	s_barrier
	s_and_saveexec_b64 s[20:21], s[4:5]
	s_cbranch_execz .LBB0_1332
	global_load_dword v6, v[156:157], off
	ds_read2st64_b32 v[0:1], v211 offset1:4
	ds_read2st64_b32 v[2:3], v211 offset0:8 offset1:12
	ds_read2st64_b32 v[4:5], v211 offset0:16 offset1:20
	s_waitcnt lgkmcnt(2)
	v_add_f32_e32 v0, 0, v0
	v_add_f32_e32 v0, v0, v1
	s_waitcnt lgkmcnt(1)
	v_add_f32_e32 v2, v0, v2
	ds_read2st64_b32 v[0:1], v211 offset0:24 offset1:28
	v_add_f32_e32 v2, v2, v3
	s_waitcnt lgkmcnt(1)
	v_add_f32_e32 v4, v2, v4
	ds_read2st64_b32 v[2:3], v211 offset0:32 offset1:36
	v_add_f32_e32 v4, v4, v5
	s_waitcnt lgkmcnt(1)
	v_add_f32_e32 v0, v4, v0
	ds_read2st64_b32 v[4:5], v211 offset0:40 offset1:44
	v_add_f32_e32 v0, v0, v1
	s_waitcnt lgkmcnt(1)
	v_add_f32_e32 v2, v0, v2
	ds_read2st64_b32 v[0:1], v211 offset0:48 offset1:52
	v_add_f32_e32 v2, v2, v3
	s_waitcnt lgkmcnt(1)
	v_add_f32_e32 v4, v2, v4
	ds_read2st64_b32 v[2:3], v211 offset0:56 offset1:60
	v_add_f32_e32 v4, v4, v5
	s_waitcnt lgkmcnt(1)
	v_add_f32_e32 v0, v4, v0
	ds_read2st64_b32 v[4:5], v211 offset0:64 offset1:68
	v_add_f32_e32 v0, v0, v1
	s_waitcnt lgkmcnt(1)
	v_add_f32_e32 v2, v0, v2
	ds_read2st64_b32 v[0:1], v211 offset0:72 offset1:76
	v_add_f32_e32 v2, v2, v3
	s_waitcnt lgkmcnt(1)
	v_add_f32_e32 v4, v2, v4
	ds_read2st64_b32 v[2:3], v211 offset0:80 offset1:84
	v_add_f32_e32 v4, v4, v5
	s_waitcnt lgkmcnt(1)
	v_add_f32_e32 v0, v4, v0
	ds_read2st64_b32 v[4:5], v211 offset0:88 offset1:92
	v_add_f32_e32 v0, v0, v1
	s_waitcnt lgkmcnt(1)
	v_add_f32_e32 v2, v0, v2
	ds_read2st64_b32 v[0:1], v211 offset0:96 offset1:100
	v_add_f32_e32 v2, v2, v3
	s_waitcnt lgkmcnt(1)
	v_add_f32_e32 v2, v2, v4
	v_add_f32_e32 v4, v2, v5
	ds_read2st64_b32 v[2:3], v211 offset0:104 offset1:108
	s_waitcnt lgkmcnt(1)
	v_add_f32_e32 v0, v4, v0
	ds_read2st64_b32 v[4:5], v211 offset0:112 offset1:116
	v_add_f32_e32 v7, v0, v1
	ds_read2st64_b32 v[0:1], v211 offset0:120 offset1:124
	s_waitcnt lgkmcnt(2)
	v_add_f32_e32 v2, v7, v2
	v_add_f32_e32 v2, v2, v3
	s_waitcnt lgkmcnt(1)
	v_add_f32_e32 v2, v2, v4
	v_add_f32_e32 v2, v2, v5
	s_waitcnt lgkmcnt(0)
	v_add_f32_e32 v0, v2, v0
	v_add_f32_e32 v0, v0, v1
	s_waitcnt vmcnt(0)
	v_add_f32_e32 v0, v0, v6
	ds_write_b32 v212, v0
